# P0: int8 weights not used until P7 or later stored nt (w_in int8 and h keep default policy)
# baseline (speedup 1.0000x reference)
; template <int NCH>
; __device__ __forceinline__ void quant_colblock(const Frame& F, const float* src, int ld_src, int nvalid, unsigned char* dst, int ld_dst, float* sb) {
;     ...
;     f32x4 sc; sc.x = am.x > 0.f ? 127.f / am.x : 0.f; sc.y = am.y > 0.f ? 127.f / am.y : 0.f; sc.z = am.z > 0.f ? 127.f / am.z : 0.f; sc.w = am.w > 0.f ? 127.f / am.w : 0.f;
;     if (w == 0 && kg == 0) *(f32x4*)(sb + n) = am * (1.f / 127.f);
;     unsigned char* db = dst + w * rows;
;     const unsigned doff = (unsigned)n * (unsigned)ld_dst + (unsigned)(16 * kg);
; #pragma unroll
;     for (int c = 0; c < NCH; ++c) { unsigned t[16][2];
;         if (c < NREG) {
; #pragma unroll
;             for (int i = 0; i < 16; ++i) { t[i][0] = h[c < NREG ? c : 0][i][0]; t[i][1] = h[c < NREG ? c : 0][i][1]; } }
;         else {
; #pragma unroll
;             for (int e = 0; e < 8; ++e) { const u32x4 q = hl[((c - 2) * 8 + e) * 512]; t[2 * e][0] = q.x; t[2 * e][1] = q.y; t[2 * e + 1][0] = q.z; t[2 * e + 1][1] = q.w; } }
; #pragma unroll
;         for (int jn = 0; jn < 4; ++jn) { const float s1 = sc[jn];
;     ...
;             u32x4 o; o.x = pack_i8x4(HV(0), HV(1), HV(2), HV(3)); o.y = pack_i8x4(HV(4), HV(5), HV(6), HV(7)); o.z = pack_i8x4(HV(8), HV(9), HV(10), HV(11)); o.w = pack_i8x4(HV(12), HV(13), HV(14), HV(15));
;     ...
;             *(u32x4*)(db + (size_t)(jn * ld_dst + c * 128) + doff) = o; }
.LBB0_14:
	s_or_b64 exec, exec, s[46:47]
	s_cmpk_gt_u32 s82, 0x1e7
	s_cselect_b64 s[84:85], -1, 0
	s_cselect_b64 s[92:93], 0, -1
	v_div_scale_f32 v34, s[44:45], v4, v4, s78
	v_rcp_f32_e32 v60, v34
	v_div_scale_f32 v61, vcc, s78, v4, s78
	v_cvt_pkrtz_f16_f32 v10, v10, v11
	v_fma_f32 v62, -v34, v60, 1.0
	v_fmac_f32_e32 v60, v62, v60
	v_mul_f32_e32 v62, v61, v60
	v_fma_f32 v157, -v34, v62, v61
	v_fmac_f32_e32 v62, v157, v60
	v_fma_f32 v34, -v34, v62, v61
	v_cvt_pkrtz_f16_f32 v18, v18, v19
	v_cvt_pkrtz_f16_f32 v14, v14, v15
	v_cvt_pkrtz_f16_f32 v12, v12, v13
	v_cvt_pkrtz_f16_f32 v13, v6, v7
	v_cvt_f32_f16_e32 v7, v10
	v_div_fmas_f32 v34, v34, v60, v62
	v_cvt_pkrtz_f16_f32 v11, v8, v9
	v_cvt_f32_f16_e32 v6, v13
	v_cvt_f32_f16_e32 v8, v14
	v_cvt_f32_f16_e32 v9, v18
	v_div_fixup_f32 v34, v34, v4, s78
	v_cmp_lt_f32_e32 vcc, 0, v4
	v_cvt_pkrtz_f16_f32 v26, v26, v27
	v_cvt_pkrtz_f16_f32 v44, v44, v45
	v_cndmask_b32_e32 v62, 0, v34, vcc
	v_mul_f32_e32 v7, v62, v7
	v_mul_f32_e32 v6, v62, v6
	v_mul_f32_e32 v8, v62, v8
	v_mul_f32_e32 v9, v62, v9
	v_rndne_f32_e32 v7, v7
	v_rndne_f32_e32 v6, v6
	v_cvt_i32_f32_e32 v7, v7
	v_rndne_f32_e32 v8, v8
	v_rndne_f32_e32 v9, v9
	v_cvt_i32_f32_e32 v6, v6
	v_cvt_i32_f32_sdwa v8, v8 dst_sel:WORD_1 dst_unused:UNUSED_PAD src0_sel:DWORD
	v_cvt_i32_f32_e32 v9, v9
	v_lshlrev_b32_e32 v7, 8, v7
	v_and_b32_e32 v7, 0xff00, v7
	v_and_b32_e32 v8, 0xff0000, v8
	v_perm_b32 v6, v9, v6, s79
	v_cvt_pkrtz_f16_f32 v45, v40, v41
	v_cvt_pkrtz_f16_f32 v40, v38, v39
	v_cvt_pkrtz_f16_f32 v30, v30, v31
	v_cvt_pkrtz_f16_f32 v22, v22, v23
	v_or3_b32 v6, v6, v7, v8
	v_cvt_f32_f16_e32 v8, v26
	v_cvt_f32_f16_e32 v7, v22
	v_cvt_f32_f16_e32 v9, v30
	v_cvt_f32_f16_e32 v15, v40
	v_mul_f32_e32 v8, v62, v8
	v_mul_f32_e32 v7, v62, v7
	v_mul_f32_e32 v9, v62, v9
	v_mul_f32_e32 v15, v62, v15
	v_rndne_f32_e32 v8, v8
	v_rndne_f32_e32 v7, v7
	v_cvt_i32_f32_e32 v8, v8
	v_rndne_f32_e32 v9, v9
	v_rndne_f32_e32 v15, v15
	v_cvt_i32_f32_e32 v7, v7
	v_cvt_i32_f32_sdwa v9, v9 dst_sel:WORD_1 dst_unused:UNUSED_PAD src0_sel:DWORD
	v_cvt_i32_f32_e32 v15, v15
	v_lshlrev_b32_e32 v8, 8, v8
	v_cvt_pkrtz_f16_f32 v63, v63, v64
	v_and_b32_e32 v8, 0xff00, v8
	v_and_b32_e32 v9, 0xff0000, v9
	v_perm_b32 v7, v15, v7, s79
	v_cvt_pkrtz_f16_f32 v71, v71, v72
	v_cvt_pkrtz_f16_f32 v67, v67, v68
	v_cvt_pkrtz_f16_f32 v42, v42, v43
	v_or3_b32 v7, v7, v8, v9
	v_cvt_f32_f16_e32 v9, v63
	v_cvt_pkrtz_f16_f32 v16, v16, v17
	v_cvt_f32_f16_e32 v8, v42
	v_cvt_f32_f16_e32 v15, v67
	v_cvt_f32_f16_e32 v17, v71
	v_mul_f32_e32 v9, v62, v9
	v_mul_f32_e32 v8, v62, v8
	v_mul_f32_e32 v15, v62, v15
	v_mul_f32_e32 v17, v62, v17
	v_rndne_f32_e32 v9, v9
	v_rndne_f32_e32 v8, v8
	v_cvt_i32_f32_e32 v9, v9
	v_rndne_f32_e32 v15, v15
	v_rndne_f32_e32 v17, v17
	v_cvt_i32_f32_e32 v8, v8
	v_cvt_i32_f32_sdwa v15, v15 dst_sel:WORD_1 dst_unused:UNUSED_PAD src0_sel:DWORD
	v_cvt_i32_f32_e32 v17, v17
	v_lshlrev_b32_e32 v9, 8, v9
	v_cvt_pkrtz_f16_f32 v79, v79, v80
	v_and_b32_e32 v9, 0xff00, v9
	v_and_b32_e32 v15, 0xff0000, v15
	v_perm_b32 v8, v17, v8, s79
	v_cvt_pkrtz_f16_f32 v87, v87, v88
	v_cvt_pkrtz_f16_f32 v83, v83, v84
	v_cvt_pkrtz_f16_f32 v75, v75, v76
	v_or3_b32 v8, v8, v9, v15
	v_cvt_f32_f16_e32 v15, v79
	v_cvt_f32_f16_e32 v9, v75
	v_cvt_f32_f16_e32 v17, v83
	v_cvt_f32_f16_e32 v19, v87
	v_div_scale_f32 v60, s[44:45], v5, v5, s78
	v_rcp_f32_e32 v61, v60
	v_mul_f32_e32 v15, v62, v15
	v_mul_f32_e32 v9, v62, v9
	v_mul_f32_e32 v17, v62, v17
	v_mul_f32_e32 v19, v62, v19
	v_rndne_f32_e32 v15, v15
	v_rndne_f32_e32 v9, v9
	v_cvt_i32_f32_e32 v15, v15
	v_rndne_f32_e32 v17, v17
	v_rndne_f32_e32 v19, v19
	v_cvt_i32_f32_e32 v9, v9
	v_cvt_i32_f32_sdwa v17, v17 dst_sel:WORD_1 dst_unused:UNUSED_PAD src0_sel:DWORD
	v_cvt_i32_f32_e32 v19, v19
	v_fma_f32 v4, -v60, v61, 1.0
	v_fmac_f32_e32 v61, v4, v61
	v_div_scale_f32 v4, vcc, s78, v5, s78
	v_mul_f32_e32 v34, v4, v61
	s_add_u32 s42, s42, s73
	v_lshlrev_b32_e32 v15, 8, v15
	v_fma_f32 v157, -v60, v34, v4
	s_addc_u32 s43, s43, 0
	v_and_b32_e32 v15, 0xff00, v15
	v_and_b32_e32 v17, 0xff0000, v17
	v_perm_b32 v9, v19, v9, s79
	v_fmac_f32_e32 v34, v157, v61
	v_lshl_add_u64 v[38:39], s[42:43], 0, v[36:37]
	v_or3_b32 v9, v9, v15, v17
	v_fma_f32 v4, -v60, v34, v4
	s_mov_b64 exec, s[84:85]
	global_store_dwordx4 v[38:39], v[6:9], off nt
	s_mov_b64 exec, s[92:93]
	global_store_dwordx4 v[38:39], v[6:9], off
	s_mov_b64 exec, -1
	v_div_fmas_f32 v4, v4, v61, v34
	v_div_fixup_f32 v4, v4, v5, s78
	v_cvt_f32_f16_sdwa v7, v10 dst_sel:DWORD dst_unused:UNUSED_PAD src0_sel:WORD_1
	v_cvt_f32_f16_sdwa v6, v13 dst_sel:DWORD dst_unused:UNUSED_PAD src0_sel:WORD_1
	v_cvt_f32_f16_sdwa v8, v14 dst_sel:DWORD dst_unused:UNUSED_PAD src0_sel:WORD_1
	v_cvt_f32_f16_sdwa v9, v18 dst_sel:DWORD dst_unused:UNUSED_PAD src0_sel:WORD_1
	v_cmp_lt_f32_e32 vcc, 0, v5
	v_cvt_f32_f16_sdwa v10, v40 dst_sel:DWORD dst_unused:UNUSED_PAD src0_sel:WORD_1
	v_div_scale_f32 v34, s[44:45], v2, v2, s78
	v_cndmask_b32_e32 v61, 0, v4, vcc
	v_mul_f32_e32 v7, v61, v7
	v_mul_f32_e32 v6, v61, v6
	v_mul_f32_e32 v8, v61, v8
	v_mul_f32_e32 v9, v61, v9
	v_rndne_f32_e32 v7, v7
	v_rndne_f32_e32 v6, v6
	v_cvt_i32_f32_e32 v7, v7
	v_rndne_f32_e32 v8, v8
	v_rndne_f32_e32 v9, v9
	v_cvt_i32_f32_e32 v6, v6
	v_cvt_i32_f32_sdwa v8, v8 dst_sel:WORD_1 dst_unused:UNUSED_PAD src0_sel:DWORD
	v_cvt_i32_f32_e32 v9, v9
	v_lshlrev_b32_e32 v7, 8, v7
	v_and_b32_e32 v7, 0xff00, v7
	v_and_b32_e32 v8, 0xff0000, v8
	v_perm_b32 v6, v9, v6, s79
	v_or3_b32 v6, v6, v7, v8
	v_cvt_f32_f16_sdwa v8, v26 dst_sel:DWORD dst_unused:UNUSED_PAD src0_sel:WORD_1
	v_cvt_f32_f16_sdwa v7, v22 dst_sel:DWORD dst_unused:UNUSED_PAD src0_sel:WORD_1
	v_cvt_f32_f16_sdwa v9, v30 dst_sel:DWORD dst_unused:UNUSED_PAD src0_sel:WORD_1
; template <int NCH>
; __device__ __forceinline__ void quant_colblock(const Frame& F, const float* src, int ld_src, int nvalid, unsigned char* dst, int ld_dst, float* sb) {
;     ...
;     for (int c = 0; c < NCH; ++c) { unsigned t[16][2];
;         if (c < NREG) {
; #pragma unroll
;             for (int i = 0; i < 16; ++i) { t[i][0] = h[c < NREG ? c : 0][i][0]; t[i][1] = h[c < NREG ? c : 0][i][1]; } }
;         else {
; #pragma unroll
;             for (int e = 0; e < 8; ++e) { const u32x4 q = hl[((c - 2) * 8 + e) * 512]; t[2 * e][0] = q.x; t[2 * e][1] = q.y; t[2 * e + 1][0] = q.z; t[2 * e + 1][1] = q.w; } }
; #pragma unroll
;         for (int jn = 0; jn < 4; ++jn) { const float s1 = sc[jn];
;     ...
;             u32x4 o; o.x = pack_i8x4(HV(0), HV(1), HV(2), HV(3)); o.y = pack_i8x4(HV(4), HV(5), HV(6), HV(7)); o.z = pack_i8x4(HV(8), HV(9), HV(10), HV(11)); o.w = pack_i8x4(HV(12), HV(13), HV(14), HV(15));
;     ...
;             *(u32x4*)(db + (size_t)(jn * ld_dst + c * 128) + doff) = o; }
	v_mul_f32_e32 v10, v61, v10
	v_mul_f32_e32 v8, v61, v8
	v_mul_f32_e32 v7, v61, v7
	v_mul_f32_e32 v9, v61, v9
	v_rndne_f32_e32 v8, v8
	v_rndne_f32_e32 v7, v7
	v_cvt_i32_f32_e32 v8, v8
	v_rndne_f32_e32 v9, v9
	v_rndne_f32_e32 v10, v10
	v_cvt_i32_f32_e32 v7, v7
	v_cvt_i32_f32_sdwa v9, v9 dst_sel:WORD_1 dst_unused:UNUSED_PAD src0_sel:DWORD
	v_cvt_i32_f32_e32 v10, v10
	v_rcp_f32_e32 v60, v34
	v_lshlrev_b32_e32 v8, 8, v8
	v_and_b32_e32 v8, 0xff00, v8
	v_and_b32_e32 v9, 0xff0000, v9
	v_perm_b32 v7, v10, v7, s79
	v_or3_b32 v7, v7, v8, v9
	v_cvt_f32_f16_sdwa v9, v63 dst_sel:DWORD dst_unused:UNUSED_PAD src0_sel:WORD_1
	v_cvt_f32_f16_sdwa v8, v42 dst_sel:DWORD dst_unused:UNUSED_PAD src0_sel:WORD_1
	v_cvt_f32_f16_sdwa v10, v67 dst_sel:DWORD dst_unused:UNUSED_PAD src0_sel:WORD_1
	v_cvt_f32_f16_sdwa v13, v71 dst_sel:DWORD dst_unused:UNUSED_PAD src0_sel:WORD_1
	v_fma_f32 v4, -v34, v60, 1.0
	v_fmac_f32_e32 v60, v4, v60
	v_div_scale_f32 v4, vcc, s78, v2, s78
	v_mul_f32_e32 v5, v4, v60
	v_mul_f32_e32 v9, v61, v9
	v_fma_f32 v157, -v34, v5, v4
	v_mul_f32_e32 v8, v61, v8
	v_mul_f32_e32 v10, v61, v10
	v_mul_f32_e32 v13, v61, v13
	v_rndne_f32_e32 v9, v9
	v_fmac_f32_e32 v5, v157, v60
	v_rndne_f32_e32 v8, v8
	v_cvt_i32_f32_e32 v9, v9
	v_rndne_f32_e32 v10, v10
	v_rndne_f32_e32 v13, v13
	v_fma_f32 v4, -v34, v5, v4
	v_cvt_i32_f32_e32 v8, v8
	v_cvt_i32_f32_sdwa v10, v10 dst_sel:WORD_1 dst_unused:UNUSED_PAD src0_sel:DWORD
	v_cvt_i32_f32_e32 v13, v13
	v_div_fmas_f32 v4, v4, v60, v5
	v_div_scale_f32 v5, s[44:45], v3, v3, s78
	v_rcp_f32_e32 v34, v5
	v_lshlrev_b32_e32 v9, 8, v9
	v_and_b32_e32 v9, 0xff00, v9
	v_and_b32_e32 v10, 0xff0000, v10
	v_perm_b32 v8, v13, v8, s79
	v_or3_b32 v8, v8, v9, v10
	v_cvt_f32_f16_sdwa v10, v79 dst_sel:DWORD dst_unused:UNUSED_PAD src0_sel:WORD_1
	v_div_fixup_f32 v4, v4, v2, s78
	v_cmp_lt_f32_e32 vcc, 0, v2
	v_fma_f32 v2, -v5, v34, 1.0
	v_cvt_f32_f16_sdwa v9, v75 dst_sel:DWORD dst_unused:UNUSED_PAD src0_sel:WORD_1
	v_cvt_f32_f16_sdwa v13, v83 dst_sel:DWORD dst_unused:UNUSED_PAD src0_sel:WORD_1
	v_cvt_f32_f16_sdwa v14, v87 dst_sel:DWORD dst_unused:UNUSED_PAD src0_sel:WORD_1
	v_cndmask_b32_e32 v60, 0, v4, vcc
	v_fmac_f32_e32 v34, v2, v34
	v_div_scale_f32 v2, vcc, s78, v3, s78
	v_mul_f32_e32 v4, v2, v34
	v_fma_f32 v157, -v5, v4, v2
	v_mul_f32_e32 v10, v61, v10
	v_fmac_f32_e32 v4, v157, v34
	v_mul_f32_e32 v9, v61, v9
	v_mul_f32_e32 v13, v61, v13
	v_mul_f32_e32 v14, v61, v14
	v_rndne_f32_e32 v10, v10
	v_fma_f32 v2, -v5, v4, v2
	v_rndne_f32_e32 v9, v9
	v_cvt_i32_f32_e32 v10, v10
	v_rndne_f32_e32 v13, v13
	v_rndne_f32_e32 v14, v14
	v_div_fmas_f32 v2, v2, v34, v4
	v_cvt_i32_f32_e32 v9, v9
	v_cvt_i32_f32_sdwa v13, v13 dst_sel:WORD_1 dst_unused:UNUSED_PAD src0_sel:DWORD
	v_cvt_i32_f32_e32 v14, v14
	v_div_fixup_f32 v2, v2, v3, s78
	v_cmp_lt_f32_e32 vcc, 0, v3
	v_lshlrev_b32_e32 v10, 8, v10
	v_and_b32_e32 v10, 0xff00, v10
	v_cndmask_b32_e32 v34, 0, v2, vcc
	v_add_co_u32_e32 v42, vcc, s80, v38
	v_and_b32_e32 v13, 0xff0000, v13
	s_nop 0
	v_addc_co_u32_e32 v43, vcc, 0, v39, vcc
	v_perm_b32 v9, v14, v9, s79
	v_add_co_u32_e32 v40, vcc, s77, v38
	v_or3_b32 v9, v9, v10, v13
	s_nop 0
	v_addc_co_u32_e32 v41, vcc, 0, v39, vcc
	v_cvt_pkrtz_f16_f32 v20, v20, v21
	s_mov_b64 exec, s[84:85]
	global_store_dwordx4 v[40:41], v[6:9], off offset:-4096 nt
	s_mov_b64 exec, s[92:93]
	global_store_dwordx4 v[40:41], v[6:9], off offset:-4096
	s_mov_b64 exec, -1
	v_cvt_pkrtz_f16_f32 v28, v28, v29
	v_cvt_pkrtz_f16_f32 v32, v32, v33
	v_cvt_f32_f16_e32 v7, v12
	v_cvt_f32_f16_e32 v6, v11
	v_cvt_f32_f16_e32 v8, v16
	v_cvt_f32_f16_e32 v9, v20
	v_mul_f32_e32 v7, v60, v7
	v_mul_f32_e32 v6, v60, v6
	v_mul_f32_e32 v8, v60, v8
	v_mul_f32_e32 v9, v60, v9
	v_rndne_f32_e32 v7, v7
	v_rndne_f32_e32 v6, v6
	v_cvt_i32_f32_e32 v7, v7
	v_rndne_f32_e32 v8, v8
	v_rndne_f32_e32 v9, v9
	v_cvt_i32_f32_e32 v6, v6
	v_cvt_i32_f32_sdwa v8, v8 dst_sel:WORD_1 dst_unused:UNUSED_PAD src0_sel:DWORD
	v_cvt_i32_f32_e32 v9, v9
	v_lshlrev_b32_e32 v7, 8, v7
	v_and_b32_e32 v7, 0xff00, v7
	v_and_b32_e32 v8, 0xff0000, v8
	v_perm_b32 v6, v9, v6, s79
	v_cvt_pkrtz_f16_f32 v24, v24, v25
	v_or3_b32 v6, v6, v7, v8
	v_cvt_f32_f16_e32 v8, v28
	v_cvt_f32_f16_e32 v7, v24
	v_cvt_f32_f16_e32 v9, v32
	v_cvt_f32_f16_e32 v10, v45
	v_mul_f32_e32 v8, v60, v8
	v_mul_f32_e32 v7, v60, v7
	v_mul_f32_e32 v9, v60, v9
	v_mul_f32_e32 v10, v60, v10
	v_rndne_f32_e32 v8, v8
	v_rndne_f32_e32 v7, v7
	v_cvt_i32_f32_e32 v8, v8
	v_rndne_f32_e32 v9, v9
	v_rndne_f32_e32 v10, v10
	v_cvt_i32_f32_e32 v7, v7
	v_cvt_i32_f32_sdwa v9, v9 dst_sel:WORD_1 dst_unused:UNUSED_PAD src0_sel:DWORD
	v_cvt_i32_f32_e32 v10, v10
	v_lshlrev_b32_e32 v8, 8, v8
	v_cvt_pkrtz_f16_f32 v65, v65, v66
	v_and_b32_e32 v8, 0xff00, v8
	v_and_b32_e32 v9, 0xff0000, v9
	v_perm_b32 v7, v10, v7, s79
	v_cvt_pkrtz_f16_f32 v73, v73, v74
	v_cvt_pkrtz_f16_f32 v69, v69, v70
	v_or3_b32 v7, v7, v8, v9
	v_cvt_f32_f16_e32 v9, v65
	v_cvt_f32_f16_e32 v8, v44
	v_cvt_f32_f16_e32 v10, v69
	v_cvt_f32_f16_e32 v13, v73
	v_mul_f32_e32 v9, v60, v9
	v_mul_f32_e32 v8, v60, v8
	v_mul_f32_e32 v10, v60, v10
	v_mul_f32_e32 v13, v60, v13
	v_rndne_f32_e32 v9, v9
	v_rndne_f32_e32 v8, v8
	v_cvt_i32_f32_e32 v9, v9
	v_rndne_f32_e32 v10, v10
	v_rndne_f32_e32 v13, v13
	v_cvt_i32_f32_e32 v8, v8
	v_cvt_i32_f32_sdwa v10, v10 dst_sel:WORD_1 dst_unused:UNUSED_PAD src0_sel:DWORD
	v_cvt_i32_f32_e32 v13, v13
	v_lshlrev_b32_e32 v9, 8, v9
	v_cvt_pkrtz_f16_f32 v81, v81, v82
	v_and_b32_e32 v9, 0xff00, v9
	v_and_b32_e32 v10, 0xff0000, v10
	v_perm_b32 v8, v13, v8, s79
	v_cvt_pkrtz_f16_f32 v89, v89, v90
	v_cvt_pkrtz_f16_f32 v85, v85, v86
	v_cvt_pkrtz_f16_f32 v77, v77, v78
	v_or3_b32 v8, v8, v9, v10
	v_cvt_f32_f16_e32 v10, v81
; template <int NCH>
; __device__ __forceinline__ void quant_colblock(const Frame& F, const float* src, int ld_src, int nvalid, unsigned char* dst, int ld_dst, float* sb) {
;     ...
;     for (int c = 0; c < NCH; ++c) { unsigned t[16][2];
;         if (c < NREG) {
; #pragma unroll
;             for (int i = 0; i < 16; ++i) { t[i][0] = h[c < NREG ? c : 0][i][0]; t[i][1] = h[c < NREG ? c : 0][i][1]; } }
;         else {
; #pragma unroll
;             for (int e = 0; e < 8; ++e) { const u32x4 q = hl[((c - 2) * 8 + e) * 512]; t[2 * e][0] = q.x; t[2 * e][1] = q.y; t[2 * e + 1][0] = q.z; t[2 * e + 1][1] = q.w; } }
; #pragma unroll
;         for (int jn = 0; jn < 4; ++jn) { const float s1 = sc[jn];
;     ...
;             u32x4 o; o.x = pack_i8x4(HV(0), HV(1), HV(2), HV(3)); o.y = pack_i8x4(HV(4), HV(5), HV(6), HV(7)); o.z = pack_i8x4(HV(8), HV(9), HV(10), HV(11)); o.w = pack_i8x4(HV(12), HV(13), HV(14), HV(15));
;     ...
;             *(u32x4*)(db + (size_t)(jn * ld_dst + c * 128) + doff) = o; }
	v_cvt_f32_f16_e32 v9, v77
	v_cvt_f32_f16_e32 v13, v85
	v_cvt_f32_f16_e32 v14, v89
	v_mul_f32_e32 v10, v60, v10
	v_mul_f32_e32 v9, v60, v9
	v_mul_f32_e32 v13, v60, v13
	v_mul_f32_e32 v14, v60, v14
	v_rndne_f32_e32 v10, v10
	v_rndne_f32_e32 v9, v9
	v_cvt_i32_f32_e32 v10, v10
	v_rndne_f32_e32 v13, v13
	v_rndne_f32_e32 v14, v14
	v_cvt_i32_f32_e32 v9, v9
	v_cvt_i32_f32_sdwa v13, v13 dst_sel:WORD_1 dst_unused:UNUSED_PAD src0_sel:DWORD
	v_cvt_i32_f32_e32 v14, v14
	v_lshlrev_b32_e32 v10, 8, v10
	v_and_b32_e32 v10, 0xff00, v10
	v_and_b32_e32 v13, 0xff0000, v13
	v_perm_b32 v9, v14, v9, s79
	v_or3_b32 v9, v9, v10, v13
	s_mov_b64 exec, s[84:85]
	global_store_dwordx4 v[40:41], v[6:9], off nt
	s_mov_b64 exec, s[92:93]
	global_store_dwordx4 v[40:41], v[6:9], off
	s_mov_b64 exec, -1
	v_cvt_f32_f16_sdwa v10, v45 dst_sel:DWORD dst_unused:UNUSED_PAD src0_sel:WORD_1
	v_cvt_pkrtz_f16_f32 v2, v155, v156
	v_cvt_f32_f16_sdwa v7, v12 dst_sel:DWORD dst_unused:UNUSED_PAD src0_sel:WORD_1
	v_cvt_f32_f16_sdwa v6, v11 dst_sel:DWORD dst_unused:UNUSED_PAD src0_sel:WORD_1
	v_cvt_f32_f16_sdwa v8, v16 dst_sel:DWORD dst_unused:UNUSED_PAD src0_sel:WORD_1
	v_cvt_f32_f16_sdwa v9, v20 dst_sel:DWORD dst_unused:UNUSED_PAD src0_sel:WORD_1
	v_mul_f32_e32 v7, v34, v7
	v_mul_f32_e32 v6, v34, v6
	v_mul_f32_e32 v8, v34, v8
	v_mul_f32_e32 v9, v34, v9
	v_rndne_f32_e32 v7, v7
	v_rndne_f32_e32 v6, v6
	v_cvt_i32_f32_e32 v7, v7
	v_rndne_f32_e32 v8, v8
	v_rndne_f32_e32 v9, v9
	v_cvt_i32_f32_e32 v6, v6
	v_cvt_i32_f32_sdwa v8, v8 dst_sel:WORD_1 dst_unused:UNUSED_PAD src0_sel:DWORD
	v_cvt_i32_f32_e32 v9, v9
	v_lshlrev_b32_e32 v7, 8, v7
	v_and_b32_e32 v7, 0xff00, v7
	v_and_b32_e32 v8, 0xff0000, v8
	v_perm_b32 v6, v9, v6, s79
	v_or3_b32 v6, v6, v7, v8
	v_cvt_f32_f16_sdwa v8, v28 dst_sel:DWORD dst_unused:UNUSED_PAD src0_sel:WORD_1
	v_cvt_f32_f16_sdwa v7, v24 dst_sel:DWORD dst_unused:UNUSED_PAD src0_sel:WORD_1
	v_cvt_f32_f16_sdwa v9, v32 dst_sel:DWORD dst_unused:UNUSED_PAD src0_sel:WORD_1
	v_mul_f32_e32 v10, v34, v10
	v_mul_f32_e32 v8, v34, v8
	v_mul_f32_e32 v7, v34, v7
	v_mul_f32_e32 v9, v34, v9
	v_rndne_f32_e32 v8, v8
	v_rndne_f32_e32 v7, v7
	v_cvt_i32_f32_e32 v8, v8
	v_rndne_f32_e32 v9, v9
	v_rndne_f32_e32 v10, v10
	v_cvt_i32_f32_e32 v7, v7
	v_cvt_i32_f32_sdwa v9, v9 dst_sel:WORD_1 dst_unused:UNUSED_PAD src0_sel:DWORD
	v_cvt_i32_f32_e32 v10, v10
	v_lshlrev_b32_e32 v8, 8, v8
	v_and_b32_e32 v8, 0xff00, v8
	v_and_b32_e32 v9, 0xff0000, v9
	v_perm_b32 v7, v10, v7, s79
	v_or3_b32 v7, v7, v8, v9
	v_cvt_f32_f16_sdwa v9, v65 dst_sel:DWORD dst_unused:UNUSED_PAD src0_sel:WORD_1
	v_cvt_f32_f16_sdwa v8, v44 dst_sel:DWORD dst_unused:UNUSED_PAD src0_sel:WORD_1
	v_cvt_f32_f16_sdwa v10, v69 dst_sel:DWORD dst_unused:UNUSED_PAD src0_sel:WORD_1
	v_cvt_f32_f16_sdwa v11, v73 dst_sel:DWORD dst_unused:UNUSED_PAD src0_sel:WORD_1
	v_mul_f32_e32 v9, v34, v9
	v_mul_f32_e32 v8, v34, v8
	v_mul_f32_e32 v10, v34, v10
	v_mul_f32_e32 v11, v34, v11
	v_rndne_f32_e32 v9, v9
	v_rndne_f32_e32 v8, v8
	v_cvt_i32_f32_e32 v9, v9
	v_rndne_f32_e32 v10, v10
	v_rndne_f32_e32 v11, v11
	v_cvt_i32_f32_e32 v8, v8
	v_cvt_i32_f32_sdwa v10, v10 dst_sel:WORD_1 dst_unused:UNUSED_PAD src0_sel:DWORD
	v_cvt_i32_f32_e32 v11, v11
	v_lshlrev_b32_e32 v9, 8, v9
	v_and_b32_e32 v9, 0xff00, v9
	v_and_b32_e32 v10, 0xff0000, v10
	v_perm_b32 v8, v11, v8, s79
	v_or3_b32 v8, v8, v9, v10
	v_cvt_f32_f16_sdwa v10, v81 dst_sel:DWORD dst_unused:UNUSED_PAD src0_sel:WORD_1
	v_cvt_f32_f16_sdwa v9, v77 dst_sel:DWORD dst_unused:UNUSED_PAD src0_sel:WORD_1
	v_cvt_f32_f16_sdwa v11, v85 dst_sel:DWORD dst_unused:UNUSED_PAD src0_sel:WORD_1
	v_cvt_f32_f16_sdwa v12, v89 dst_sel:DWORD dst_unused:UNUSED_PAD src0_sel:WORD_1
	v_mul_f32_e32 v10, v34, v10
	v_mul_f32_e32 v9, v34, v9
	v_mul_f32_e32 v11, v34, v11
	v_mul_f32_e32 v12, v34, v12
	v_rndne_f32_e32 v10, v10
	v_rndne_f32_e32 v9, v9
	v_cvt_i32_f32_e32 v10, v10
	v_rndne_f32_e32 v11, v11
	v_rndne_f32_e32 v12, v12
	v_cvt_i32_f32_e32 v9, v9
	v_cvt_i32_f32_sdwa v11, v11 dst_sel:WORD_1 dst_unused:UNUSED_PAD src0_sel:DWORD
	v_cvt_i32_f32_e32 v12, v12
	v_lshlrev_b32_e32 v10, 8, v10
	v_and_b32_e32 v10, 0xff00, v10
	v_and_b32_e32 v11, 0xff0000, v11
	v_perm_b32 v9, v12, v9, s79
	v_add_co_u32_e32 v44, vcc, s81, v38
	v_or3_b32 v9, v9, v10, v11
	s_nop 0
	v_addc_co_u32_e32 v45, vcc, 0, v39, vcc
	v_cvt_pkrtz_f16_f32 v153, v153, v154
	v_cvt_pkrtz_f16_f32 v3, v151, v152
	v_cvt_pkrtz_f16_f32 v149, v149, v150
	v_cvt_pkrtz_f16_f32 v4, v147, v148
	v_cvt_pkrtz_f16_f32 v145, v145, v146
	v_cvt_pkrtz_f16_f32 v5, v143, v144
	v_cvt_pkrtz_f16_f32 v141, v141, v142
	v_cvt_pkrtz_f16_f32 v109, v109, v140
	v_cvt_pkrtz_f16_f32 v136, v136, v137
	v_cvt_pkrtz_f16_f32 v113, v113, v135
	v_cvt_pkrtz_f16_f32 v133, v133, v134
	v_cvt_pkrtz_f16_f32 v117, v117, v132
	v_cvt_pkrtz_f16_f32 v130, v130, v131
	v_cvt_pkrtz_f16_f32 v120, v120, v129
	v_cvt_pkrtz_f16_f32 v127, v127, v128
	v_cvt_pkrtz_f16_f32 v125, v125, v126
	v_cvt_pkrtz_f16_f32 v123, v123, v124
	v_cvt_pkrtz_f16_f32 v121, v121, v122
	v_cvt_pkrtz_f16_f32 v118, v118, v119
	v_cvt_pkrtz_f16_f32 v115, v115, v116
	v_cvt_pkrtz_f16_f32 v112, v112, v114
	v_cvt_pkrtz_f16_f32 v110, v110, v111
	v_cvt_pkrtz_f16_f32 v107, v107, v108
	v_cvt_pkrtz_f16_f32 v105, v105, v106
	v_cvt_pkrtz_f16_f32 v103, v103, v104
	v_cvt_pkrtz_f16_f32 v101, v101, v102
	v_cvt_pkrtz_f16_f32 v99, v99, v100
	v_cvt_pkrtz_f16_f32 v97, v97, v98
	v_cvt_pkrtz_f16_f32 v95, v95, v96
	v_cvt_pkrtz_f16_f32 v93, v93, v94
	v_cvt_pkrtz_f16_f32 v91, v91, v92
	s_mov_b64 exec, s[84:85]
	global_store_dwordx4 v[44:45], v[6:9], off nt
	s_mov_b64 exec, s[92:93]
	global_store_dwordx4 v[44:45], v[6:9], off
	s_mov_b64 exec, -1
	s_nop 1
	v_cvt_f32_f16_e32 v7, v95
	v_cvt_f32_f16_e32 v6, v91
; template <int NCH>
; __device__ __forceinline__ void quant_colblock(const Frame& F, const float* src, int ld_src, int nvalid, unsigned char* dst, int ld_dst, float* sb) {
;     ...
;     for (int c = 0; c < NCH; ++c) { unsigned t[16][2];
;         if (c < NREG) {
; #pragma unroll
;             for (int i = 0; i < 16; ++i) { t[i][0] = h[c < NREG ? c : 0][i][0]; t[i][1] = h[c < NREG ? c : 0][i][1]; } }
;         else {
; #pragma unroll
;             for (int e = 0; e < 8; ++e) { const u32x4 q = hl[((c - 2) * 8 + e) * 512]; t[2 * e][0] = q.x; t[2 * e][1] = q.y; t[2 * e + 1][0] = q.z; t[2 * e + 1][1] = q.w; } }
; #pragma unroll
;         for (int jn = 0; jn < 4; ++jn) { const float s1 = sc[jn];
;     ...
;             u32x4 o; o.x = pack_i8x4(HV(0), HV(1), HV(2), HV(3)); o.y = pack_i8x4(HV(4), HV(5), HV(6), HV(7)); o.z = pack_i8x4(HV(8), HV(9), HV(10), HV(11)); o.w = pack_i8x4(HV(12), HV(13), HV(14), HV(15));
;     ...
;             *(u32x4*)(db + (size_t)(jn * ld_dst + c * 128) + doff) = o; }
	v_cvt_f32_f16_e32 v8, v99
	v_cvt_f32_f16_e32 v9, v103
	v_mul_f32_e32 v7, v62, v7
	v_mul_f32_e32 v6, v62, v6
	v_mul_f32_e32 v8, v62, v8
	v_mul_f32_e32 v9, v62, v9
	v_rndne_f32_e32 v7, v7
	v_rndne_f32_e32 v6, v6
	v_cvt_i32_f32_e32 v7, v7
	v_rndne_f32_e32 v8, v8
	v_rndne_f32_e32 v9, v9
	v_cvt_i32_f32_e32 v6, v6
	v_cvt_i32_f32_sdwa v8, v8 dst_sel:WORD_1 dst_unused:UNUSED_PAD src0_sel:DWORD
	v_cvt_i32_f32_e32 v9, v9
	v_lshlrev_b32_e32 v7, 8, v7
	v_and_b32_e32 v7, 0xff00, v7
	v_and_b32_e32 v8, 0xff0000, v8
	v_perm_b32 v6, v9, v6, s79
	v_or3_b32 v6, v6, v7, v8
	v_cvt_f32_f16_e32 v8, v112
	v_cvt_f32_f16_e32 v7, v107
	v_cvt_f32_f16_e32 v9, v118
	v_cvt_f32_f16_e32 v10, v123
	v_mul_f32_e32 v8, v62, v8
	v_mul_f32_e32 v7, v62, v7
	v_mul_f32_e32 v9, v62, v9
	v_mul_f32_e32 v10, v62, v10
	v_rndne_f32_e32 v8, v8
	v_rndne_f32_e32 v7, v7
	v_cvt_i32_f32_e32 v8, v8
	v_rndne_f32_e32 v9, v9
	v_rndne_f32_e32 v10, v10
	v_cvt_i32_f32_e32 v7, v7
	v_cvt_i32_f32_sdwa v9, v9 dst_sel:WORD_1 dst_unused:UNUSED_PAD src0_sel:DWORD
	v_cvt_i32_f32_e32 v10, v10
	v_lshlrev_b32_e32 v8, 8, v8
	v_and_b32_e32 v8, 0xff00, v8
	v_and_b32_e32 v9, 0xff0000, v9
	v_perm_b32 v7, v10, v7, s79
	v_or3_b32 v7, v7, v8, v9
	v_cvt_f32_f16_e32 v9, v130
	v_cvt_f32_f16_e32 v8, v127
	v_cvt_f32_f16_e32 v10, v133
	v_cvt_f32_f16_e32 v11, v136
	v_mul_f32_e32 v9, v62, v9
	v_mul_f32_e32 v8, v62, v8
	v_mul_f32_e32 v10, v62, v10
	v_mul_f32_e32 v11, v62, v11
	v_rndne_f32_e32 v9, v9
	v_rndne_f32_e32 v8, v8
	v_cvt_i32_f32_e32 v9, v9
	v_rndne_f32_e32 v10, v10
	v_rndne_f32_e32 v11, v11
	v_cvt_i32_f32_e32 v8, v8
	v_cvt_i32_f32_sdwa v10, v10 dst_sel:WORD_1 dst_unused:UNUSED_PAD src0_sel:DWORD
	v_cvt_i32_f32_e32 v11, v11
	v_lshlrev_b32_e32 v9, 8, v9
	v_and_b32_e32 v9, 0xff00, v9
	v_and_b32_e32 v10, 0xff0000, v10
	v_perm_b32 v8, v11, v8, s79
	v_or3_b32 v8, v8, v9, v10
	v_cvt_f32_f16_e32 v10, v145
	v_cvt_f32_f16_e32 v9, v141
	v_cvt_f32_f16_e32 v11, v149
	v_cvt_f32_f16_e32 v12, v153
	v_mul_f32_e32 v10, v62, v10
	v_mul_f32_e32 v9, v62, v9
	v_mul_f32_e32 v11, v62, v11
	v_mul_f32_e32 v12, v62, v12
	v_rndne_f32_e32 v10, v10
	v_rndne_f32_e32 v9, v9
	v_cvt_i32_f32_e32 v10, v10
	v_rndne_f32_e32 v11, v11
	v_rndne_f32_e32 v12, v12
	v_cvt_i32_f32_e32 v9, v9
	v_cvt_i32_f32_sdwa v11, v11 dst_sel:WORD_1 dst_unused:UNUSED_PAD src0_sel:DWORD
	v_cvt_i32_f32_e32 v12, v12
	v_lshlrev_b32_e32 v10, 8, v10
	v_and_b32_e32 v10, 0xff00, v10
	v_and_b32_e32 v11, 0xff0000, v11
	v_perm_b32 v9, v12, v9, s79
	v_or3_b32 v9, v9, v10, v11
	s_mov_b64 exec, s[84:85]
	global_store_dwordx4 v[38:39], v[6:9], off offset:128 nt
	s_mov_b64 exec, s[92:93]
	global_store_dwordx4 v[38:39], v[6:9], off offset:128
	s_mov_b64 exec, -1
	v_cvt_f32_f16_sdwa v10, v123 dst_sel:DWORD dst_unused:UNUSED_PAD src0_sel:WORD_1
	v_cvt_f32_f16_sdwa v11, v136 dst_sel:DWORD dst_unused:UNUSED_PAD src0_sel:WORD_1
	v_cvt_f32_f16_sdwa v7, v95 dst_sel:DWORD dst_unused:UNUSED_PAD src0_sel:WORD_1
	v_cvt_f32_f16_sdwa v6, v91 dst_sel:DWORD dst_unused:UNUSED_PAD src0_sel:WORD_1
	v_cvt_f32_f16_sdwa v8, v99 dst_sel:DWORD dst_unused:UNUSED_PAD src0_sel:WORD_1
	v_cvt_f32_f16_sdwa v9, v103 dst_sel:DWORD dst_unused:UNUSED_PAD src0_sel:WORD_1
	v_mul_f32_e32 v7, v61, v7
	v_mul_f32_e32 v6, v61, v6
	v_mul_f32_e32 v8, v61, v8
	v_mul_f32_e32 v9, v61, v9
	v_rndne_f32_e32 v7, v7
	v_rndne_f32_e32 v6, v6
	v_cvt_i32_f32_e32 v7, v7
	v_rndne_f32_e32 v8, v8
	v_rndne_f32_e32 v9, v9
	v_cvt_i32_f32_e32 v6, v6
	v_cvt_i32_f32_sdwa v8, v8 dst_sel:WORD_1 dst_unused:UNUSED_PAD src0_sel:DWORD
	v_cvt_i32_f32_e32 v9, v9
	v_lshlrev_b32_e32 v7, 8, v7
	v_and_b32_e32 v7, 0xff00, v7
	v_and_b32_e32 v8, 0xff0000, v8
	v_perm_b32 v6, v9, v6, s79
	v_or3_b32 v6, v6, v7, v8
	v_cvt_f32_f16_sdwa v8, v112 dst_sel:DWORD dst_unused:UNUSED_PAD src0_sel:WORD_1
	v_cvt_f32_f16_sdwa v7, v107 dst_sel:DWORD dst_unused:UNUSED_PAD src0_sel:WORD_1
	v_cvt_f32_f16_sdwa v9, v118 dst_sel:DWORD dst_unused:UNUSED_PAD src0_sel:WORD_1
	v_mul_f32_e32 v10, v61, v10
	v_mul_f32_e32 v8, v61, v8
	v_mul_f32_e32 v7, v61, v7
	v_mul_f32_e32 v9, v61, v9
	v_rndne_f32_e32 v8, v8
	v_rndne_f32_e32 v7, v7
	v_cvt_i32_f32_e32 v8, v8
	v_rndne_f32_e32 v9, v9
	v_rndne_f32_e32 v10, v10
	v_cvt_i32_f32_e32 v7, v7
	v_cvt_i32_f32_sdwa v9, v9 dst_sel:WORD_1 dst_unused:UNUSED_PAD src0_sel:DWORD
	v_cvt_i32_f32_e32 v10, v10
	v_lshlrev_b32_e32 v8, 8, v8
	v_and_b32_e32 v8, 0xff00, v8
	v_and_b32_e32 v9, 0xff0000, v9
	v_perm_b32 v7, v10, v7, s79
	v_or3_b32 v7, v7, v8, v9
	v_cvt_f32_f16_sdwa v9, v130 dst_sel:DWORD dst_unused:UNUSED_PAD src0_sel:WORD_1
	v_cvt_f32_f16_sdwa v8, v127 dst_sel:DWORD dst_unused:UNUSED_PAD src0_sel:WORD_1
	v_cvt_f32_f16_sdwa v10, v133 dst_sel:DWORD dst_unused:UNUSED_PAD src0_sel:WORD_1
	v_mul_f32_e32 v11, v61, v11
	v_mul_f32_e32 v9, v61, v9
	v_mul_f32_e32 v8, v61, v8
	v_mul_f32_e32 v10, v61, v10
	v_rndne_f32_e32 v9, v9
	v_rndne_f32_e32 v8, v8
	v_cvt_i32_f32_e32 v9, v9
	v_rndne_f32_e32 v10, v10
	v_rndne_f32_e32 v11, v11
	v_cvt_i32_f32_e32 v8, v8
	v_cvt_i32_f32_sdwa v10, v10 dst_sel:WORD_1 dst_unused:UNUSED_PAD src0_sel:DWORD
	v_cvt_i32_f32_e32 v11, v11
	v_lshlrev_b32_e32 v9, 8, v9
	v_and_b32_e32 v9, 0xff00, v9
	v_and_b32_e32 v10, 0xff0000, v10
	v_perm_b32 v8, v11, v8, s79
	v_or3_b32 v8, v8, v9, v10
	v_cvt_f32_f16_sdwa v10, v145 dst_sel:DWORD dst_unused:UNUSED_PAD src0_sel:WORD_1
	v_cvt_f32_f16_sdwa v9, v141 dst_sel:DWORD dst_unused:UNUSED_PAD src0_sel:WORD_1
	v_cvt_f32_f16_sdwa v11, v149 dst_sel:DWORD dst_unused:UNUSED_PAD src0_sel:WORD_1
	v_cvt_f32_f16_sdwa v12, v153 dst_sel:DWORD dst_unused:UNUSED_PAD src0_sel:WORD_1
	v_mul_f32_e32 v10, v61, v10
	v_mul_f32_e32 v9, v61, v9
	v_mul_f32_e32 v11, v61, v11
	v_mul_f32_e32 v12, v61, v12
	v_rndne_f32_e32 v10, v10
; template <int NCH>
; __device__ __forceinline__ void quant_colblock(const Frame& F, const float* src, int ld_src, int nvalid, unsigned char* dst, int ld_dst, float* sb) {
;     ...
;     for (int c = 0; c < NCH; ++c) { unsigned t[16][2];
;         if (c < NREG) {
; #pragma unroll
;             for (int i = 0; i < 16; ++i) { t[i][0] = h[c < NREG ? c : 0][i][0]; t[i][1] = h[c < NREG ? c : 0][i][1]; } }
;         else {
; #pragma unroll
;             for (int e = 0; e < 8; ++e) { const u32x4 q = hl[((c - 2) * 8 + e) * 512]; t[2 * e][0] = q.x; t[2 * e][1] = q.y; t[2 * e + 1][0] = q.z; t[2 * e + 1][1] = q.w; } }
; #pragma unroll
;         for (int jn = 0; jn < 4; ++jn) { const float s1 = sc[jn];
;     ...
;             u32x4 o; o.x = pack_i8x4(HV(0), HV(1), HV(2), HV(3)); o.y = pack_i8x4(HV(4), HV(5), HV(6), HV(7)); o.z = pack_i8x4(HV(8), HV(9), HV(10), HV(11)); o.w = pack_i8x4(HV(12), HV(13), HV(14), HV(15));
;     ...
;             *(u32x4*)(db + (size_t)(jn * ld_dst + c * 128) + doff) = o; }
	v_rndne_f32_e32 v9, v9
	v_cvt_i32_f32_e32 v10, v10
	v_rndne_f32_e32 v11, v11
	v_rndne_f32_e32 v12, v12
	v_cvt_i32_f32_e32 v9, v9
	v_cvt_i32_f32_sdwa v11, v11 dst_sel:WORD_1 dst_unused:UNUSED_PAD src0_sel:DWORD
	v_cvt_i32_f32_e32 v12, v12
	v_lshlrev_b32_e32 v10, 8, v10
	v_and_b32_e32 v10, 0xff00, v10
	v_and_b32_e32 v11, 0xff0000, v11
	v_perm_b32 v9, v12, v9, s79
	v_or3_b32 v9, v9, v10, v11
	s_mov_b64 exec, s[84:85]
	global_store_dwordx4 v[42:43], v[6:9], off offset:128 nt
	s_mov_b64 exec, s[92:93]
	global_store_dwordx4 v[42:43], v[6:9], off offset:128
	s_mov_b64 exec, -1
	v_cvt_f32_f16_e32 v10, v125
	v_cvt_f32_f16_e32 v11, v109
	v_cvt_f32_f16_e32 v7, v97
	v_cvt_f32_f16_e32 v6, v93
	v_cvt_f32_f16_e32 v8, v101
	v_cvt_f32_f16_e32 v9, v105
	v_mul_f32_e32 v7, v60, v7
	v_mul_f32_e32 v6, v60, v6
	v_mul_f32_e32 v8, v60, v8
	v_mul_f32_e32 v9, v60, v9
	v_rndne_f32_e32 v7, v7
	v_rndne_f32_e32 v6, v6
	v_cvt_i32_f32_e32 v7, v7
	v_rndne_f32_e32 v8, v8
	v_rndne_f32_e32 v9, v9
	v_cvt_i32_f32_e32 v6, v6
	v_cvt_i32_f32_sdwa v8, v8 dst_sel:WORD_1 dst_unused:UNUSED_PAD src0_sel:DWORD
	v_cvt_i32_f32_e32 v9, v9
	v_lshlrev_b32_e32 v7, 8, v7
	v_and_b32_e32 v7, 0xff00, v7
	v_and_b32_e32 v8, 0xff0000, v8
	v_perm_b32 v6, v9, v6, s79
	v_or3_b32 v6, v6, v7, v8
	v_cvt_f32_f16_e32 v8, v115
	v_cvt_f32_f16_e32 v7, v110
	v_cvt_f32_f16_e32 v9, v121
	v_mul_f32_e32 v10, v60, v10
	v_mul_f32_e32 v8, v60, v8
	v_mul_f32_e32 v7, v60, v7
	v_mul_f32_e32 v9, v60, v9
	v_rndne_f32_e32 v8, v8
	v_rndne_f32_e32 v7, v7
	v_cvt_i32_f32_e32 v8, v8
	v_rndne_f32_e32 v9, v9
	v_rndne_f32_e32 v10, v10
	v_cvt_i32_f32_e32 v7, v7
	v_cvt_i32_f32_sdwa v9, v9 dst_sel:WORD_1 dst_unused:UNUSED_PAD src0_sel:DWORD
	v_cvt_i32_f32_e32 v10, v10
	v_lshlrev_b32_e32 v8, 8, v8
	v_and_b32_e32 v8, 0xff00, v8
	v_and_b32_e32 v9, 0xff0000, v9
	v_perm_b32 v7, v10, v7, s79
	v_or3_b32 v7, v7, v8, v9
	v_cvt_f32_f16_e32 v9, v117
	v_cvt_f32_f16_e32 v8, v120
	v_cvt_f32_f16_e32 v10, v113
	v_mul_f32_e32 v11, v60, v11
	v_mul_f32_e32 v9, v60, v9
	v_mul_f32_e32 v8, v60, v8
	v_mul_f32_e32 v10, v60, v10
	v_rndne_f32_e32 v9, v9
	v_rndne_f32_e32 v8, v8
	v_cvt_i32_f32_e32 v9, v9
	v_rndne_f32_e32 v10, v10
	v_rndne_f32_e32 v11, v11
	v_cvt_i32_f32_e32 v8, v8
	v_cvt_i32_f32_sdwa v10, v10 dst_sel:WORD_1 dst_unused:UNUSED_PAD src0_sel:DWORD
	v_cvt_i32_f32_e32 v11, v11
	v_lshlrev_b32_e32 v9, 8, v9
	v_and_b32_e32 v9, 0xff00, v9
	v_and_b32_e32 v10, 0xff0000, v10
	v_perm_b32 v8, v11, v8, s79
	v_or3_b32 v8, v8, v9, v10
	v_cvt_f32_f16_e32 v10, v4
	v_cvt_f32_f16_e32 v9, v5
	v_cvt_f32_f16_e32 v11, v3
	v_cvt_f32_f16_e32 v12, v2
	v_mul_f32_e32 v10, v60, v10
	v_mul_f32_e32 v9, v60, v9
	v_mul_f32_e32 v11, v60, v11
	v_mul_f32_e32 v12, v60, v12
	v_rndne_f32_e32 v10, v10
	v_rndne_f32_e32 v9, v9
	v_cvt_i32_f32_e32 v10, v10
	v_rndne_f32_e32 v11, v11
	v_rndne_f32_e32 v12, v12
	v_cvt_i32_f32_e32 v9, v9
	v_cvt_i32_f32_sdwa v11, v11 dst_sel:WORD_1 dst_unused:UNUSED_PAD src0_sel:DWORD
	v_cvt_i32_f32_e32 v12, v12
	v_lshlrev_b32_e32 v10, 8, v10
	v_and_b32_e32 v10, 0xff00, v10
	v_and_b32_e32 v11, 0xff0000, v11
	v_perm_b32 v9, v12, v9, s79
	v_or3_b32 v9, v9, v10, v11
	s_mov_b64 exec, s[84:85]
	global_store_dwordx4 v[40:41], v[6:9], off offset:128 nt
	s_mov_b64 exec, s[92:93]
	global_store_dwordx4 v[40:41], v[6:9], off offset:128
	s_mov_b64 exec, -1
	v_cvt_f32_f16_sdwa v10, v125 dst_sel:DWORD dst_unused:UNUSED_PAD src0_sel:WORD_1
	v_cvt_f32_f16_sdwa v4, v4 dst_sel:DWORD dst_unused:UNUSED_PAD src0_sel:WORD_1
	v_cvt_f32_f16_sdwa v7, v97 dst_sel:DWORD dst_unused:UNUSED_PAD src0_sel:WORD_1
	v_cvt_f32_f16_sdwa v6, v93 dst_sel:DWORD dst_unused:UNUSED_PAD src0_sel:WORD_1
	v_cvt_f32_f16_sdwa v8, v101 dst_sel:DWORD dst_unused:UNUSED_PAD src0_sel:WORD_1
	v_cvt_f32_f16_sdwa v9, v105 dst_sel:DWORD dst_unused:UNUSED_PAD src0_sel:WORD_1
	v_mul_f32_e32 v7, v34, v7
	v_mul_f32_e32 v6, v34, v6
	v_mul_f32_e32 v8, v34, v8
	v_mul_f32_e32 v9, v34, v9
	v_rndne_f32_e32 v7, v7
	v_rndne_f32_e32 v6, v6
	v_cvt_i32_f32_e32 v7, v7
	v_rndne_f32_e32 v8, v8
	v_rndne_f32_e32 v9, v9
	v_cvt_i32_f32_e32 v6, v6
	v_cvt_i32_f32_sdwa v8, v8 dst_sel:WORD_1 dst_unused:UNUSED_PAD src0_sel:DWORD
	v_cvt_i32_f32_e32 v9, v9
	v_lshlrev_b32_e32 v7, 8, v7
	v_and_b32_e32 v7, 0xff00, v7
	v_and_b32_e32 v8, 0xff0000, v8
	v_perm_b32 v6, v9, v6, s79
	v_or3_b32 v6, v6, v7, v8
	v_cvt_f32_f16_sdwa v8, v115 dst_sel:DWORD dst_unused:UNUSED_PAD src0_sel:WORD_1
	v_cvt_f32_f16_sdwa v7, v110 dst_sel:DWORD dst_unused:UNUSED_PAD src0_sel:WORD_1
	v_cvt_f32_f16_sdwa v9, v121 dst_sel:DWORD dst_unused:UNUSED_PAD src0_sel:WORD_1
	v_mul_f32_e32 v10, v34, v10
	v_mul_f32_e32 v8, v34, v8
	v_mul_f32_e32 v7, v34, v7
	v_mul_f32_e32 v9, v34, v9
	v_rndne_f32_e32 v8, v8
	v_rndne_f32_e32 v7, v7
	v_cvt_i32_f32_e32 v8, v8
	v_rndne_f32_e32 v9, v9
	v_rndne_f32_e32 v10, v10
	v_cvt_i32_f32_e32 v7, v7
	v_cvt_i32_f32_sdwa v9, v9 dst_sel:WORD_1 dst_unused:UNUSED_PAD src0_sel:DWORD
	v_cvt_i32_f32_e32 v10, v10
	v_lshlrev_b32_e32 v8, 8, v8
	v_and_b32_e32 v8, 0xff00, v8
	v_and_b32_e32 v9, 0xff0000, v9
	v_perm_b32 v7, v10, v7, s79
	v_or3_b32 v7, v7, v8, v9
	v_cvt_f32_f16_sdwa v9, v117 dst_sel:DWORD dst_unused:UNUSED_PAD src0_sel:WORD_1
	v_cvt_f32_f16_sdwa v8, v120 dst_sel:DWORD dst_unused:UNUSED_PAD src0_sel:WORD_1
	v_cvt_f32_f16_sdwa v10, v113 dst_sel:DWORD dst_unused:UNUSED_PAD src0_sel:WORD_1
	v_cvt_f32_f16_sdwa v11, v109 dst_sel:DWORD dst_unused:UNUSED_PAD src0_sel:WORD_1
	v_cvt_f32_f16_sdwa v5, v5 dst_sel:DWORD dst_unused:UNUSED_PAD src0_sel:WORD_1
	v_cvt_f32_f16_sdwa v3, v3 dst_sel:DWORD dst_unused:UNUSED_PAD src0_sel:WORD_1
	v_cvt_f32_f16_sdwa v2, v2 dst_sel:DWORD dst_unused:UNUSED_PAD src0_sel:WORD_1
	v_mul_f32_e32 v9, v34, v9
	v_mul_f32_e32 v4, v34, v4
; template <int NCH>
; __device__ __forceinline__ void quant_colblock(const Frame& F, const float* src, int ld_src, int nvalid, unsigned char* dst, int ld_dst, float* sb) {
;     ...
;     for (int c = 0; c < NCH; ++c) { unsigned t[16][2];
;         if (c < NREG) {
; #pragma unroll
;             for (int i = 0; i < 16; ++i) { t[i][0] = h[c < NREG ? c : 0][i][0]; t[i][1] = h[c < NREG ? c : 0][i][1]; } }
;         else {
; #pragma unroll
;             for (int e = 0; e < 8; ++e) { const u32x4 q = hl[((c - 2) * 8 + e) * 512]; t[2 * e][0] = q.x; t[2 * e][1] = q.y; t[2 * e + 1][0] = q.z; t[2 * e + 1][1] = q.w; } }
; #pragma unroll
;         for (int jn = 0; jn < 4; ++jn) { const float s1 = sc[jn];
;     ...
;             u32x4 o; o.x = pack_i8x4(HV(0), HV(1), HV(2), HV(3)); o.y = pack_i8x4(HV(4), HV(5), HV(6), HV(7)); o.z = pack_i8x4(HV(8), HV(9), HV(10), HV(11)); o.w = pack_i8x4(HV(12), HV(13), HV(14), HV(15));
;     ...
;             *(u32x4*)(db + (size_t)(jn * ld_dst + c * 128) + doff) = o; }
	v_mul_f32_e32 v8, v34, v8
	v_mul_f32_e32 v10, v34, v10
	v_mul_f32_e32 v11, v34, v11
	v_rndne_f32_e32 v9, v9
	v_mul_f32_e32 v5, v34, v5
	v_mul_f32_e32 v3, v34, v3
	v_mul_f32_e32 v2, v34, v2
	v_rndne_f32_e32 v4, v4
	v_rndne_f32_e32 v8, v8
	v_cvt_i32_f32_e32 v9, v9
	v_rndne_f32_e32 v10, v10
	v_rndne_f32_e32 v11, v11
	v_rndne_f32_e32 v5, v5
	v_cvt_i32_f32_e32 v4, v4
	v_rndne_f32_e32 v3, v3
	v_rndne_f32_e32 v2, v2
	v_cvt_i32_f32_e32 v8, v8
	v_cvt_i32_f32_sdwa v10, v10 dst_sel:WORD_1 dst_unused:UNUSED_PAD src0_sel:DWORD
	v_cvt_i32_f32_e32 v11, v11
	v_cvt_i32_f32_e32 v5, v5
	v_cvt_i32_f32_sdwa v3, v3 dst_sel:WORD_1 dst_unused:UNUSED_PAD src0_sel:DWORD
	v_cvt_i32_f32_e32 v2, v2
	v_lshlrev_b32_e32 v9, 8, v9
	v_lshlrev_b32_e32 v4, 8, v4
	v_and_b32_e32 v9, 0xff00, v9
	v_and_b32_e32 v10, 0xff0000, v10
	v_perm_b32 v8, v11, v8, s79
	v_and_b32_e32 v4, 0xff00, v4
	v_and_b32_e32 v3, 0xff0000, v3
	v_perm_b32 v2, v2, v5, s79
	v_or3_b32 v8, v8, v9, v10
	v_or3_b32 v9, v2, v4, v3
	s_mov_b64 exec, s[84:85]
	global_store_dwordx4 v[44:45], v[6:9], off offset:128 nt
	s_mov_b64 exec, s[92:93]
	global_store_dwordx4 v[44:45], v[6:9], off offset:128
	s_mov_b64 exec, -1
	ds_read_b128 v[2:5], v46 offset:61440
	ds_read_b128 v[6:9], v46 offset:53248
	ds_read_b128 v[26:29], v46 offset:12288
	ds_read_b128 v[30:33], v46 offset:4096
	ds_read_b128 v[10:13], v46 offset:45056
	ds_read_b128 v[14:17], v46 offset:36864
	ds_read_b128 v[18:21], v46 offset:28672
	ds_read_b128 v[22:25], v46 offset:20480
	s_waitcnt lgkmcnt(4)
	v_cvt_f32_f16_e32 v64, v32
	v_cvt_f32_f16_e32 v63, v30
	v_cvt_f32_f16_e32 v65, v26
	v_cvt_f32_f16_e32 v66, v28
	v_mul_f32_e32 v64, v62, v64
	v_mul_f32_e32 v63, v62, v63
	v_mul_f32_e32 v65, v62, v65
	v_mul_f32_e32 v66, v62, v66
	v_rndne_f32_e32 v64, v64
	v_rndne_f32_e32 v63, v63
	v_cvt_i32_f32_e32 v64, v64
	v_rndne_f32_e32 v65, v65
	v_rndne_f32_e32 v66, v66
	v_cvt_i32_f32_e32 v63, v63
	v_cvt_i32_f32_sdwa v65, v65 dst_sel:WORD_1 dst_unused:UNUSED_PAD src0_sel:DWORD
	v_cvt_i32_f32_e32 v66, v66
	v_lshlrev_b32_e32 v64, 8, v64
	v_and_b32_e32 v64, 0xff00, v64
	v_and_b32_e32 v65, 0xff0000, v65
	v_perm_b32 v63, v66, v63, s79
	v_or3_b32 v64, v63, v64, v65
	s_waitcnt lgkmcnt(0)
	v_cvt_f32_f16_e32 v65, v24
	v_cvt_f32_f16_e32 v63, v22
	v_cvt_f32_f16_e32 v66, v18
	v_cvt_f32_f16_e32 v67, v20
	v_mul_f32_e32 v65, v62, v65
	v_mul_f32_e32 v63, v62, v63
	v_mul_f32_e32 v66, v62, v66
	v_mul_f32_e32 v67, v62, v67
	v_rndne_f32_e32 v65, v65
	v_rndne_f32_e32 v63, v63
	v_cvt_i32_f32_e32 v65, v65
	v_rndne_f32_e32 v66, v66
	v_rndne_f32_e32 v67, v67
	v_cvt_i32_f32_e32 v63, v63
	v_cvt_i32_f32_sdwa v66, v66 dst_sel:WORD_1 dst_unused:UNUSED_PAD src0_sel:DWORD
	v_cvt_i32_f32_e32 v67, v67
	v_lshlrev_b32_e32 v65, 8, v65
	v_and_b32_e32 v65, 0xff00, v65
	v_and_b32_e32 v66, 0xff0000, v66
	v_perm_b32 v63, v67, v63, s79
	v_or3_b32 v65, v63, v65, v66
	v_cvt_f32_f16_e32 v66, v16
	v_cvt_f32_f16_e32 v63, v14
	v_cvt_f32_f16_e32 v67, v10
	v_cvt_f32_f16_e32 v68, v12
	v_mul_f32_e32 v66, v62, v66
	v_mul_f32_e32 v63, v62, v63
	v_mul_f32_e32 v67, v62, v67
	v_mul_f32_e32 v68, v62, v68
	v_rndne_f32_e32 v66, v66
	v_rndne_f32_e32 v63, v63
	v_cvt_i32_f32_e32 v66, v66
	v_rndne_f32_e32 v67, v67
	v_rndne_f32_e32 v68, v68
	v_cvt_i32_f32_e32 v63, v63
	v_cvt_i32_f32_sdwa v67, v67 dst_sel:WORD_1 dst_unused:UNUSED_PAD src0_sel:DWORD
	v_cvt_i32_f32_e32 v68, v68
	v_lshlrev_b32_e32 v66, 8, v66
	v_and_b32_e32 v66, 0xff00, v66
	v_and_b32_e32 v67, 0xff0000, v67
	v_perm_b32 v63, v68, v63, s79
	v_or3_b32 v66, v63, v66, v67
	v_cvt_f32_f16_e32 v67, v8
	v_cvt_f32_f16_e32 v63, v6
	v_cvt_f32_f16_e32 v68, v2
	v_cvt_f32_f16_e32 v69, v4
	v_cvt_f32_f16_sdwa v8, v8 dst_sel:DWORD dst_unused:UNUSED_PAD src0_sel:WORD_1
	v_cvt_f32_f16_sdwa v6, v6 dst_sel:DWORD dst_unused:UNUSED_PAD src0_sel:WORD_1
	v_cvt_f32_f16_sdwa v2, v2 dst_sel:DWORD dst_unused:UNUSED_PAD src0_sel:WORD_1
	v_cvt_f32_f16_sdwa v4, v4 dst_sel:DWORD dst_unused:UNUSED_PAD src0_sel:WORD_1
	v_mul_f32_e32 v67, v62, v67
	v_mul_f32_e32 v63, v62, v63
	v_mul_f32_e32 v68, v62, v68
	v_mul_f32_e32 v69, v62, v69
	v_rndne_f32_e32 v67, v67
	v_mul_f32_e32 v8, v61, v8
	v_rndne_f32_e32 v63, v63
	v_cvt_i32_f32_e32 v67, v67
	v_rndne_f32_e32 v68, v68
	v_rndne_f32_e32 v69, v69
	v_mul_f32_e32 v6, v61, v6
	v_mul_f32_e32 v2, v61, v2
	v_mul_f32_e32 v4, v61, v4
	v_rndne_f32_e32 v8, v8
	v_cvt_i32_f32_e32 v63, v63
	v_cvt_i32_f32_sdwa v68, v68 dst_sel:WORD_1 dst_unused:UNUSED_PAD src0_sel:DWORD
	v_cvt_i32_f32_e32 v69, v69
	v_rndne_f32_e32 v6, v6
	v_cvt_i32_f32_e32 v8, v8
	v_rndne_f32_e32 v2, v2
	v_rndne_f32_e32 v4, v4
	v_cvt_i32_f32_e32 v6, v6
	v_cvt_i32_f32_sdwa v2, v2 dst_sel:WORD_1 dst_unused:UNUSED_PAD src0_sel:DWORD
	v_cvt_i32_f32_e32 v4, v4
	v_lshlrev_b32_e32 v67, 8, v67
	v_and_b32_e32 v67, 0xff00, v67
	v_and_b32_e32 v68, 0xff0000, v68
	v_perm_b32 v63, v69, v63, s79
	v_lshlrev_b32_e32 v8, 8, v8
	v_or3_b32 v67, v63, v67, v68
	v_cvt_f32_f16_sdwa v32, v32 dst_sel:DWORD dst_unused:UNUSED_PAD src0_sel:WORD_1
	v_cvt_f32_f16_sdwa v24, v24 dst_sel:DWORD dst_unused:UNUSED_PAD src0_sel:WORD_1
	v_cvt_f32_f16_sdwa v16, v16 dst_sel:DWORD dst_unused:UNUSED_PAD src0_sel:WORD_1
	v_and_b32_e32 v8, 0xff00, v8
	v_and_b32_e32 v2, 0xff0000, v2
	v_perm_b32 v4, v4, v6, s79
	s_mov_b64 exec, s[84:85]
	global_store_dwordx4 v[38:39], v[64:67], off offset:256 nt
	s_mov_b64 exec, s[92:93]
	global_store_dwordx4 v[38:39], v[64:67], off offset:256
	s_mov_b64 exec, -1
	v_cvt_f32_f16_sdwa v30, v30 dst_sel:DWORD dst_unused:UNUSED_PAD src0_sel:WORD_1
	v_cvt_f32_f16_sdwa v26, v26 dst_sel:DWORD dst_unused:UNUSED_PAD src0_sel:WORD_1
	v_cvt_f32_f16_sdwa v28, v28 dst_sel:DWORD dst_unused:UNUSED_PAD src0_sel:WORD_1
; template <int NCH>
; __device__ __forceinline__ void quant_colblock(const Frame& F, const float* src, int ld_src, int nvalid, unsigned char* dst, int ld_dst, float* sb) {
;     ...
;     for (int c = 0; c < NCH; ++c) { unsigned t[16][2];
;         if (c < NREG) {
; #pragma unroll
;             for (int i = 0; i < 16; ++i) { t[i][0] = h[c < NREG ? c : 0][i][0]; t[i][1] = h[c < NREG ? c : 0][i][1]; } }
;         else {
; #pragma unroll
;             for (int e = 0; e < 8; ++e) { const u32x4 q = hl[((c - 2) * 8 + e) * 512]; t[2 * e][0] = q.x; t[2 * e][1] = q.y; t[2 * e + 1][0] = q.z; t[2 * e + 1][1] = q.w; } }
; #pragma unroll
;         for (int jn = 0; jn < 4; ++jn) { const float s1 = sc[jn];
;     ...
;             u32x4 o; o.x = pack_i8x4(HV(0), HV(1), HV(2), HV(3)); o.y = pack_i8x4(HV(4), HV(5), HV(6), HV(7)); o.z = pack_i8x4(HV(8), HV(9), HV(10), HV(11)); o.w = pack_i8x4(HV(12), HV(13), HV(14), HV(15));
;     ...
;             *(u32x4*)(db + (size_t)(jn * ld_dst + c * 128) + doff) = o; }
	v_cvt_f32_f16_sdwa v22, v22 dst_sel:DWORD dst_unused:UNUSED_PAD src0_sel:WORD_1
	v_cvt_f32_f16_sdwa v18, v18 dst_sel:DWORD dst_unused:UNUSED_PAD src0_sel:WORD_1
	v_cvt_f32_f16_sdwa v20, v20 dst_sel:DWORD dst_unused:UNUSED_PAD src0_sel:WORD_1
	v_cvt_f32_f16_sdwa v14, v14 dst_sel:DWORD dst_unused:UNUSED_PAD src0_sel:WORD_1
	v_cvt_f32_f16_sdwa v10, v10 dst_sel:DWORD dst_unused:UNUSED_PAD src0_sel:WORD_1
	v_cvt_f32_f16_sdwa v12, v12 dst_sel:DWORD dst_unused:UNUSED_PAD src0_sel:WORD_1
	v_or3_b32 v67, v4, v8, v2
	v_cvt_f32_f16_e32 v4, v33
	v_cvt_f32_f16_e32 v2, v31
	v_cvt_f32_f16_e32 v6, v27
	v_cvt_f32_f16_e32 v8, v29
	v_mul_f32_e32 v32, v61, v32
	v_mul_f32_e32 v24, v61, v24
	v_mul_f32_e32 v16, v61, v16
	v_mul_f32_e32 v30, v61, v30
	v_mul_f32_e32 v26, v61, v26
	v_mul_f32_e32 v28, v61, v28
	v_rndne_f32_e32 v32, v32
	v_mul_f32_e32 v22, v61, v22
	v_mul_f32_e32 v18, v61, v18
	v_mul_f32_e32 v20, v61, v20
	v_rndne_f32_e32 v24, v24
	v_mul_f32_e32 v14, v61, v14
	v_mul_f32_e32 v10, v61, v10
	v_mul_f32_e32 v12, v61, v12
	v_rndne_f32_e32 v16, v16
	v_mul_f32_e32 v4, v60, v4
	v_rndne_f32_e32 v30, v30
	v_cvt_i32_f32_e32 v32, v32
	v_rndne_f32_e32 v26, v26
	v_rndne_f32_e32 v28, v28
	v_rndne_f32_e32 v22, v22
	v_cvt_i32_f32_e32 v24, v24
	v_rndne_f32_e32 v18, v18
	v_rndne_f32_e32 v20, v20
	v_rndne_f32_e32 v14, v14
	v_cvt_i32_f32_e32 v16, v16
	v_rndne_f32_e32 v10, v10
	v_rndne_f32_e32 v12, v12
	v_mul_f32_e32 v2, v60, v2
	v_mul_f32_e32 v6, v60, v6
	v_mul_f32_e32 v8, v60, v8
	v_rndne_f32_e32 v4, v4
	v_cvt_i32_f32_e32 v30, v30
	v_cvt_i32_f32_sdwa v26, v26 dst_sel:WORD_1 dst_unused:UNUSED_PAD src0_sel:DWORD
	v_cvt_i32_f32_e32 v28, v28
	v_cvt_i32_f32_e32 v22, v22
	v_cvt_i32_f32_sdwa v18, v18 dst_sel:WORD_1 dst_unused:UNUSED_PAD src0_sel:DWORD
	v_cvt_i32_f32_e32 v20, v20
	v_cvt_i32_f32_e32 v14, v14
	v_cvt_i32_f32_sdwa v10, v10 dst_sel:WORD_1 dst_unused:UNUSED_PAD src0_sel:DWORD
	v_cvt_i32_f32_e32 v12, v12
	v_rndne_f32_e32 v2, v2
	v_cvt_i32_f32_e32 v4, v4
	v_rndne_f32_e32 v6, v6
	v_rndne_f32_e32 v8, v8
	v_cvt_i32_f32_e32 v2, v2
	v_cvt_i32_f32_sdwa v6, v6 dst_sel:WORD_1 dst_unused:UNUSED_PAD src0_sel:DWORD
	v_cvt_i32_f32_e32 v8, v8
	v_lshlrev_b32_e32 v32, 8, v32
	v_lshlrev_b32_e32 v24, 8, v24
	v_lshlrev_b32_e32 v16, 8, v16
	v_and_b32_e32 v32, 0xff00, v32
	v_and_b32_e32 v26, 0xff0000, v26
	v_perm_b32 v28, v28, v30, s79
	v_and_b32_e32 v24, 0xff00, v24
	v_and_b32_e32 v18, 0xff0000, v18
	v_perm_b32 v20, v20, v22, s79
	v_and_b32_e32 v16, 0xff00, v16
	v_and_b32_e32 v10, 0xff0000, v10
	v_perm_b32 v12, v12, v14, s79
	v_lshlrev_b32_e32 v4, 8, v4
	v_or3_b32 v64, v28, v32, v26
	v_or3_b32 v65, v20, v24, v18
	v_or3_b32 v66, v12, v16, v10
	v_and_b32_e32 v4, 0xff00, v4
	v_and_b32_e32 v6, 0xff0000, v6
	v_perm_b32 v2, v8, v2, s79
	s_mov_b64 exec, s[84:85]
	global_store_dwordx4 v[42:43], v[64:67], off offset:256 nt
	s_mov_b64 exec, s[92:93]
	global_store_dwordx4 v[42:43], v[64:67], off offset:256
	s_mov_b64 exec, -1
	v_cvt_f32_f16_e32 v8, v21
	v_mul_f32_e32 v8, v60, v8
	v_or3_b32 v64, v2, v4, v6
	v_cvt_f32_f16_e32 v4, v25
	v_cvt_f32_f16_e32 v2, v23
	v_cvt_f32_f16_e32 v6, v19
	v_rndne_f32_e32 v8, v8
	v_mul_f32_e32 v4, v60, v4
	v_mul_f32_e32 v2, v60, v2
	v_mul_f32_e32 v6, v60, v6
	v_rndne_f32_e32 v4, v4
	v_rndne_f32_e32 v2, v2
	v_cvt_i32_f32_e32 v4, v4
	v_rndne_f32_e32 v6, v6
	v_cvt_i32_f32_e32 v2, v2
	v_cvt_i32_f32_sdwa v6, v6 dst_sel:WORD_1 dst_unused:UNUSED_PAD src0_sel:DWORD
	v_cvt_i32_f32_e32 v8, v8
	v_lshlrev_b32_e32 v4, 8, v4
	v_and_b32_e32 v4, 0xff00, v4
	v_and_b32_e32 v6, 0xff0000, v6
	v_perm_b32 v2, v8, v2, s79
	v_or3_b32 v65, v2, v4, v6
	v_cvt_f32_f16_e32 v4, v17
	v_cvt_f32_f16_e32 v2, v15
	v_cvt_f32_f16_e32 v6, v11
	v_cvt_f32_f16_e32 v8, v13
	v_mul_f32_e32 v4, v60, v4
	v_mul_f32_e32 v2, v60, v2
	v_mul_f32_e32 v6, v60, v6
	v_mul_f32_e32 v8, v60, v8
	v_rndne_f32_e32 v4, v4
	v_rndne_f32_e32 v2, v2
	v_cvt_i32_f32_e32 v4, v4
	v_rndne_f32_e32 v6, v6
	v_rndne_f32_e32 v8, v8
	v_cvt_i32_f32_e32 v2, v2
	v_cvt_i32_f32_sdwa v6, v6 dst_sel:WORD_1 dst_unused:UNUSED_PAD src0_sel:DWORD
	v_cvt_i32_f32_e32 v8, v8
	v_lshlrev_b32_e32 v4, 8, v4
	v_and_b32_e32 v4, 0xff00, v4
	v_and_b32_e32 v6, 0xff0000, v6
	v_perm_b32 v2, v8, v2, s79
	v_or3_b32 v66, v2, v4, v6
	v_cvt_f32_f16_e32 v4, v9
	v_cvt_f32_f16_e32 v2, v7
	v_cvt_f32_f16_e32 v6, v3
	v_cvt_f32_f16_e32 v8, v5
	v_mul_f32_e32 v4, v60, v4
	v_mul_f32_e32 v2, v60, v2
	v_mul_f32_e32 v6, v60, v6
	v_mul_f32_e32 v8, v60, v8
	v_rndne_f32_e32 v4, v4
	v_rndne_f32_e32 v2, v2
	v_cvt_i32_f32_e32 v4, v4
	v_rndne_f32_e32 v6, v6
	v_rndne_f32_e32 v8, v8
	v_cvt_i32_f32_e32 v2, v2
	v_cvt_i32_f32_sdwa v6, v6 dst_sel:WORD_1 dst_unused:UNUSED_PAD src0_sel:DWORD
	v_cvt_i32_f32_e32 v8, v8
	v_lshlrev_b32_e32 v4, 8, v4
	v_and_b32_e32 v4, 0xff00, v4
	v_and_b32_e32 v6, 0xff0000, v6
	v_perm_b32 v2, v8, v2, s79
	v_or3_b32 v67, v2, v4, v6
	v_cvt_f32_f16_sdwa v4, v33 dst_sel:DWORD dst_unused:UNUSED_PAD src0_sel:WORD_1
	v_cvt_f32_f16_sdwa v2, v31 dst_sel:DWORD dst_unused:UNUSED_PAD src0_sel:WORD_1
	v_cvt_f32_f16_sdwa v6, v27 dst_sel:DWORD dst_unused:UNUSED_PAD src0_sel:WORD_1
	v_cvt_f32_f16_sdwa v8, v29 dst_sel:DWORD dst_unused:UNUSED_PAD src0_sel:WORD_1
	v_mul_f32_e32 v4, v34, v4
	v_mul_f32_e32 v2, v34, v2
	v_mul_f32_e32 v6, v34, v6
	v_mul_f32_e32 v8, v34, v8
	v_rndne_f32_e32 v4, v4
	v_rndne_f32_e32 v2, v2
	v_cvt_i32_f32_e32 v4, v4
	v_rndne_f32_e32 v6, v6
	v_rndne_f32_e32 v8, v8
	v_cvt_i32_f32_e32 v2, v2
	v_cvt_i32_f32_sdwa v6, v6 dst_sel:WORD_1 dst_unused:UNUSED_PAD src0_sel:DWORD
	v_cvt_i32_f32_e32 v8, v8
	v_lshlrev_b32_e32 v4, 8, v4
	v_and_b32_e32 v4, 0xff00, v4
	v_and_b32_e32 v6, 0xff0000, v6
	v_perm_b32 v2, v8, v2, s79
	v_or3_b32 v18, v2, v4, v6
; template <int NCH>
; __device__ __forceinline__ void quant_colblock(const Frame& F, const float* src, int ld_src, int nvalid, unsigned char* dst, int ld_dst, float* sb) {
;     ...
;     for (int c = 0; c < NCH; ++c) { unsigned t[16][2];
;         if (c < NREG) {
; #pragma unroll
;             for (int i = 0; i < 16; ++i) { t[i][0] = h[c < NREG ? c : 0][i][0]; t[i][1] = h[c < NREG ? c : 0][i][1]; } }
;         else {
; #pragma unroll
;             for (int e = 0; e < 8; ++e) { const u32x4 q = hl[((c - 2) * 8 + e) * 512]; t[2 * e][0] = q.x; t[2 * e][1] = q.y; t[2 * e + 1][0] = q.z; t[2 * e + 1][1] = q.w; } }
; #pragma unroll
;         for (int jn = 0; jn < 4; ++jn) { const float s1 = sc[jn];
;     ...
;             u32x4 o; o.x = pack_i8x4(HV(0), HV(1), HV(2), HV(3)); o.y = pack_i8x4(HV(4), HV(5), HV(6), HV(7)); o.z = pack_i8x4(HV(8), HV(9), HV(10), HV(11)); o.w = pack_i8x4(HV(12), HV(13), HV(14), HV(15));
;     ...
;             *(u32x4*)(db + (size_t)(jn * ld_dst + c * 128) + doff) = o; }
	v_cvt_f32_f16_sdwa v4, v25 dst_sel:DWORD dst_unused:UNUSED_PAD src0_sel:WORD_1
	v_cvt_f32_f16_sdwa v2, v23 dst_sel:DWORD dst_unused:UNUSED_PAD src0_sel:WORD_1
	v_cvt_f32_f16_sdwa v6, v19 dst_sel:DWORD dst_unused:UNUSED_PAD src0_sel:WORD_1
	v_cvt_f32_f16_sdwa v8, v21 dst_sel:DWORD dst_unused:UNUSED_PAD src0_sel:WORD_1
	v_mul_f32_e32 v4, v34, v4
	v_mul_f32_e32 v2, v34, v2
	v_mul_f32_e32 v6, v34, v6
	v_mul_f32_e32 v8, v34, v8
	v_rndne_f32_e32 v4, v4
	v_rndne_f32_e32 v2, v2
	v_cvt_i32_f32_e32 v4, v4
	v_rndne_f32_e32 v6, v6
	v_rndne_f32_e32 v8, v8
	v_cvt_i32_f32_e32 v2, v2
	v_cvt_i32_f32_sdwa v6, v6 dst_sel:WORD_1 dst_unused:UNUSED_PAD src0_sel:DWORD
	v_cvt_i32_f32_e32 v8, v8
	v_lshlrev_b32_e32 v4, 8, v4
	v_and_b32_e32 v4, 0xff00, v4
	v_and_b32_e32 v6, 0xff0000, v6
	v_perm_b32 v2, v8, v2, s79
	v_or3_b32 v19, v2, v4, v6
	v_cvt_f32_f16_sdwa v4, v17 dst_sel:DWORD dst_unused:UNUSED_PAD src0_sel:WORD_1
	v_cvt_f32_f16_sdwa v2, v15 dst_sel:DWORD dst_unused:UNUSED_PAD src0_sel:WORD_1
	v_cvt_f32_f16_sdwa v6, v11 dst_sel:DWORD dst_unused:UNUSED_PAD src0_sel:WORD_1
	v_cvt_f32_f16_sdwa v8, v13 dst_sel:DWORD dst_unused:UNUSED_PAD src0_sel:WORD_1
	v_mul_f32_e32 v4, v34, v4
	v_mul_f32_e32 v2, v34, v2
	v_mul_f32_e32 v6, v34, v6
	v_mul_f32_e32 v8, v34, v8
	v_rndne_f32_e32 v4, v4
	v_rndne_f32_e32 v2, v2
	v_cvt_i32_f32_e32 v4, v4
	v_rndne_f32_e32 v6, v6
	v_rndne_f32_e32 v8, v8
	v_cvt_i32_f32_e32 v2, v2
	v_cvt_i32_f32_sdwa v6, v6 dst_sel:WORD_1 dst_unused:UNUSED_PAD src0_sel:DWORD
	v_cvt_i32_f32_e32 v8, v8
	v_lshlrev_b32_e32 v4, 8, v4
	v_and_b32_e32 v4, 0xff00, v4
	v_and_b32_e32 v6, 0xff0000, v6
	v_perm_b32 v2, v8, v2, s79
	v_or3_b32 v20, v2, v4, v6
	v_cvt_f32_f16_sdwa v4, v9 dst_sel:DWORD dst_unused:UNUSED_PAD src0_sel:WORD_1
	v_cvt_f32_f16_sdwa v2, v7 dst_sel:DWORD dst_unused:UNUSED_PAD src0_sel:WORD_1
	v_cvt_f32_f16_sdwa v3, v3 dst_sel:DWORD dst_unused:UNUSED_PAD src0_sel:WORD_1
	v_cvt_f32_f16_sdwa v5, v5 dst_sel:DWORD dst_unused:UNUSED_PAD src0_sel:WORD_1
	v_mul_f32_e32 v4, v34, v4
	v_mul_f32_e32 v2, v34, v2
	v_mul_f32_e32 v3, v34, v3
	v_mul_f32_e32 v5, v34, v5
	v_rndne_f32_e32 v4, v4
	v_rndne_f32_e32 v2, v2
	v_cvt_i32_f32_e32 v4, v4
	v_rndne_f32_e32 v3, v3
	v_rndne_f32_e32 v5, v5
	v_cvt_i32_f32_e32 v2, v2
	v_cvt_i32_f32_sdwa v3, v3 dst_sel:WORD_1 dst_unused:UNUSED_PAD src0_sel:DWORD
	v_cvt_i32_f32_e32 v5, v5
	v_lshlrev_b32_e32 v4, 8, v4
	v_and_b32_e32 v4, 0xff00, v4
	v_and_b32_e32 v3, 0xff0000, v3
	v_perm_b32 v2, v5, v2, s79
	v_or3_b32 v21, v2, v4, v3
	s_mov_b64 exec, s[84:85]
	global_store_dwordx4 v[40:41], v[64:67], off offset:256 nt
	s_mov_b64 exec, s[92:93]
	global_store_dwordx4 v[40:41], v[64:67], off offset:256
	s_mov_b64 exec, -1
	s_mov_b64 exec, s[84:85]
	global_store_dwordx4 v[44:45], v[18:21], off offset:256 nt
	s_mov_b64 exec, s[92:93]
	global_store_dwordx4 v[44:45], v[18:21], off offset:256
	s_mov_b64 exec, -1
	ds_read_b128 v[30:33], v48
	ds_read_b128 v[26:29], v49
	ds_read_b128 v[22:25], v50
	ds_read_b128 v[18:21], v51
	ds_read_b128 v[14:17], v52
	ds_read_b128 v[10:13], v53
	ds_read_b128 v[6:9], v54
	ds_read_b128 v[2:5], v55
	s_waitcnt lgkmcnt(7)
	v_cvt_f32_f16_e32 v64, v32
	v_cvt_f32_f16_e32 v63, v30
	s_waitcnt lgkmcnt(6)
	v_cvt_f32_f16_e32 v65, v26
	v_cvt_f32_f16_e32 v66, v28
	v_mul_f32_e32 v64, v62, v64
	v_mul_f32_e32 v63, v62, v63
	v_mul_f32_e32 v65, v62, v65
	v_mul_f32_e32 v66, v62, v66
	v_rndne_f32_e32 v64, v64
	v_rndne_f32_e32 v63, v63
	v_cvt_i32_f32_e32 v64, v64
	v_rndne_f32_e32 v65, v65
	v_rndne_f32_e32 v66, v66
	v_cvt_i32_f32_e32 v63, v63
	v_cvt_i32_f32_sdwa v65, v65 dst_sel:WORD_1 dst_unused:UNUSED_PAD src0_sel:DWORD
	v_cvt_i32_f32_e32 v66, v66
	v_lshlrev_b32_e32 v64, 8, v64
	v_and_b32_e32 v64, 0xff00, v64
	v_and_b32_e32 v65, 0xff0000, v65
	v_perm_b32 v63, v66, v63, s79
	v_or3_b32 v64, v63, v64, v65
	s_waitcnt lgkmcnt(5)
	v_cvt_f32_f16_e32 v65, v24
	v_cvt_f32_f16_e32 v63, v22
	s_waitcnt lgkmcnt(4)
	v_cvt_f32_f16_e32 v66, v18
	v_cvt_f32_f16_e32 v67, v20
	v_mul_f32_e32 v65, v62, v65
	v_mul_f32_e32 v63, v62, v63
	v_mul_f32_e32 v66, v62, v66
	v_mul_f32_e32 v67, v62, v67
	v_rndne_f32_e32 v65, v65
	v_rndne_f32_e32 v63, v63
	v_cvt_i32_f32_e32 v65, v65
	v_rndne_f32_e32 v66, v66
	v_rndne_f32_e32 v67, v67
	v_cvt_i32_f32_e32 v63, v63
	v_cvt_i32_f32_sdwa v66, v66 dst_sel:WORD_1 dst_unused:UNUSED_PAD src0_sel:DWORD
	v_cvt_i32_f32_e32 v67, v67
	v_lshlrev_b32_e32 v65, 8, v65
	v_and_b32_e32 v65, 0xff00, v65
	v_and_b32_e32 v66, 0xff0000, v66
	v_perm_b32 v63, v67, v63, s79
	v_or3_b32 v65, v63, v65, v66
	s_waitcnt lgkmcnt(3)
	v_cvt_f32_f16_e32 v66, v16
	v_cvt_f32_f16_e32 v63, v14
	s_waitcnt lgkmcnt(2)
	v_cvt_f32_f16_e32 v67, v10
	v_cvt_f32_f16_e32 v68, v12
	v_mul_f32_e32 v66, v62, v66
	v_mul_f32_e32 v63, v62, v63
	v_mul_f32_e32 v67, v62, v67
	v_mul_f32_e32 v68, v62, v68
	v_rndne_f32_e32 v66, v66
	v_rndne_f32_e32 v63, v63
	v_cvt_i32_f32_e32 v66, v66
	v_rndne_f32_e32 v67, v67
	v_rndne_f32_e32 v68, v68
	v_cvt_i32_f32_e32 v63, v63
	v_cvt_i32_f32_sdwa v67, v67 dst_sel:WORD_1 dst_unused:UNUSED_PAD src0_sel:DWORD
	v_cvt_i32_f32_e32 v68, v68
	v_lshlrev_b32_e32 v66, 8, v66
	v_and_b32_e32 v66, 0xff00, v66
	v_and_b32_e32 v67, 0xff0000, v67
	v_perm_b32 v63, v68, v63, s79
	v_or3_b32 v66, v63, v66, v67
	s_waitcnt lgkmcnt(1)
	v_cvt_f32_f16_e32 v67, v8
	v_cvt_f32_f16_e32 v63, v6
	s_waitcnt lgkmcnt(0)
; template <int NCH>
; __device__ __forceinline__ void quant_colblock(const Frame& F, const float* src, int ld_src, int nvalid, unsigned char* dst, int ld_dst, float* sb) {
;     ...
;     for (int c = 0; c < NCH; ++c) { unsigned t[16][2];
;         if (c < NREG) {
; #pragma unroll
;             for (int i = 0; i < 16; ++i) { t[i][0] = h[c < NREG ? c : 0][i][0]; t[i][1] = h[c < NREG ? c : 0][i][1]; } }
;         else {
; #pragma unroll
;             for (int e = 0; e < 8; ++e) { const u32x4 q = hl[((c - 2) * 8 + e) * 512]; t[2 * e][0] = q.x; t[2 * e][1] = q.y; t[2 * e + 1][0] = q.z; t[2 * e + 1][1] = q.w; } }
; #pragma unroll
;         for (int jn = 0; jn < 4; ++jn) { const float s1 = sc[jn];
;     ...
;             u32x4 o; o.x = pack_i8x4(HV(0), HV(1), HV(2), HV(3)); o.y = pack_i8x4(HV(4), HV(5), HV(6), HV(7)); o.z = pack_i8x4(HV(8), HV(9), HV(10), HV(11)); o.w = pack_i8x4(HV(12), HV(13), HV(14), HV(15));
;     ...
;             *(u32x4*)(db + (size_t)(jn * ld_dst + c * 128) + doff) = o; }
	v_cvt_f32_f16_e32 v68, v2
	v_cvt_f32_f16_e32 v69, v4
	v_cvt_f32_f16_sdwa v8, v8 dst_sel:DWORD dst_unused:UNUSED_PAD src0_sel:WORD_1
	v_cvt_f32_f16_sdwa v6, v6 dst_sel:DWORD dst_unused:UNUSED_PAD src0_sel:WORD_1
	v_cvt_f32_f16_sdwa v2, v2 dst_sel:DWORD dst_unused:UNUSED_PAD src0_sel:WORD_1
	v_cvt_f32_f16_sdwa v4, v4 dst_sel:DWORD dst_unused:UNUSED_PAD src0_sel:WORD_1
	v_mul_f32_e32 v67, v62, v67
	v_mul_f32_e32 v63, v62, v63
	v_mul_f32_e32 v68, v62, v68
	v_mul_f32_e32 v62, v62, v69
	v_rndne_f32_e32 v67, v67
	v_mul_f32_e32 v8, v61, v8
	v_rndne_f32_e32 v63, v63
	v_cvt_i32_f32_e32 v67, v67
	v_rndne_f32_e32 v68, v68
	v_rndne_f32_e32 v62, v62
	v_mul_f32_e32 v6, v61, v6
	v_mul_f32_e32 v2, v61, v2
	v_mul_f32_e32 v4, v61, v4
	v_rndne_f32_e32 v8, v8
	v_cvt_i32_f32_e32 v63, v63
	v_cvt_i32_f32_sdwa v68, v68 dst_sel:WORD_1 dst_unused:UNUSED_PAD src0_sel:DWORD
	v_cvt_i32_f32_e32 v62, v62
	v_rndne_f32_e32 v6, v6
	v_cvt_i32_f32_e32 v8, v8
	v_rndne_f32_e32 v2, v2
	v_rndne_f32_e32 v4, v4
	v_cvt_i32_f32_e32 v6, v6
	v_cvt_i32_f32_sdwa v2, v2 dst_sel:WORD_1 dst_unused:UNUSED_PAD src0_sel:DWORD
	v_cvt_i32_f32_e32 v4, v4
	v_lshlrev_b32_e32 v67, 8, v67
	v_and_b32_e32 v67, 0xff00, v67
	v_and_b32_e32 v68, 0xff0000, v68
	v_perm_b32 v62, v62, v63, s79
	v_lshlrev_b32_e32 v8, 8, v8
	v_or3_b32 v67, v62, v67, v68
	v_cvt_f32_f16_sdwa v32, v32 dst_sel:DWORD dst_unused:UNUSED_PAD src0_sel:WORD_1
	v_cvt_f32_f16_sdwa v24, v24 dst_sel:DWORD dst_unused:UNUSED_PAD src0_sel:WORD_1
	v_cvt_f32_f16_sdwa v16, v16 dst_sel:DWORD dst_unused:UNUSED_PAD src0_sel:WORD_1
	v_and_b32_e32 v8, 0xff00, v8
	v_and_b32_e32 v2, 0xff0000, v2
	v_perm_b32 v4, v4, v6, s79
	s_mov_b64 exec, s[84:85]
	global_store_dwordx4 v[38:39], v[64:67], off offset:384 nt
	s_mov_b64 exec, s[92:93]
	global_store_dwordx4 v[38:39], v[64:67], off offset:384
	s_mov_b64 exec, -1
	v_cvt_f32_f16_sdwa v30, v30 dst_sel:DWORD dst_unused:UNUSED_PAD src0_sel:WORD_1
	v_cvt_f32_f16_sdwa v26, v26 dst_sel:DWORD dst_unused:UNUSED_PAD src0_sel:WORD_1
	v_cvt_f32_f16_sdwa v28, v28 dst_sel:DWORD dst_unused:UNUSED_PAD src0_sel:WORD_1
	v_cvt_f32_f16_sdwa v22, v22 dst_sel:DWORD dst_unused:UNUSED_PAD src0_sel:WORD_1
	v_cvt_f32_f16_sdwa v18, v18 dst_sel:DWORD dst_unused:UNUSED_PAD src0_sel:WORD_1
	v_cvt_f32_f16_sdwa v20, v20 dst_sel:DWORD dst_unused:UNUSED_PAD src0_sel:WORD_1
	v_cvt_f32_f16_sdwa v14, v14 dst_sel:DWORD dst_unused:UNUSED_PAD src0_sel:WORD_1
	v_cvt_f32_f16_sdwa v10, v10 dst_sel:DWORD dst_unused:UNUSED_PAD src0_sel:WORD_1
	v_cvt_f32_f16_sdwa v12, v12 dst_sel:DWORD dst_unused:UNUSED_PAD src0_sel:WORD_1
	v_or3_b32 v65, v4, v8, v2
	v_cvt_f32_f16_e32 v4, v33
	v_cvt_f32_f16_e32 v2, v31
	v_cvt_f32_f16_e32 v6, v27
	v_cvt_f32_f16_e32 v8, v29
	v_mul_f32_e32 v32, v61, v32
	v_mul_f32_e32 v24, v61, v24
	v_mul_f32_e32 v16, v61, v16
	v_mul_f32_e32 v30, v61, v30
	v_mul_f32_e32 v26, v61, v26
	v_mul_f32_e32 v28, v61, v28
	v_rndne_f32_e32 v32, v32
	v_mul_f32_e32 v22, v61, v22
	v_mul_f32_e32 v18, v61, v18
	v_mul_f32_e32 v20, v61, v20
	v_rndne_f32_e32 v24, v24
	v_mul_f32_e32 v14, v61, v14
	v_mul_f32_e32 v10, v61, v10
	v_mul_f32_e32 v12, v61, v12
	v_rndne_f32_e32 v16, v16
	v_mul_f32_e32 v4, v60, v4
	v_rndne_f32_e32 v30, v30
	v_cvt_i32_f32_e32 v32, v32
	v_rndne_f32_e32 v26, v26
	v_rndne_f32_e32 v28, v28
	v_rndne_f32_e32 v22, v22
	v_cvt_i32_f32_e32 v24, v24
	v_rndne_f32_e32 v18, v18
	v_rndne_f32_e32 v20, v20
	v_rndne_f32_e32 v14, v14
	v_cvt_i32_f32_e32 v16, v16
	v_rndne_f32_e32 v10, v10
	v_rndne_f32_e32 v12, v12
	v_mul_f32_e32 v2, v60, v2
	v_mul_f32_e32 v6, v60, v6
	v_mul_f32_e32 v8, v60, v8
	v_rndne_f32_e32 v4, v4
	v_cvt_i32_f32_e32 v30, v30
	v_cvt_i32_f32_sdwa v26, v26 dst_sel:WORD_1 dst_unused:UNUSED_PAD src0_sel:DWORD
	v_cvt_i32_f32_e32 v28, v28
	v_cvt_i32_f32_e32 v22, v22
	v_cvt_i32_f32_sdwa v18, v18 dst_sel:WORD_1 dst_unused:UNUSED_PAD src0_sel:DWORD
	v_cvt_i32_f32_e32 v20, v20
	v_cvt_i32_f32_e32 v14, v14
	v_cvt_i32_f32_sdwa v10, v10 dst_sel:WORD_1 dst_unused:UNUSED_PAD src0_sel:DWORD
	v_cvt_i32_f32_e32 v12, v12
	v_rndne_f32_e32 v2, v2
	v_cvt_i32_f32_e32 v4, v4
	v_rndne_f32_e32 v6, v6
	v_rndne_f32_e32 v8, v8
	v_cvt_i32_f32_e32 v2, v2
	v_cvt_i32_f32_sdwa v6, v6 dst_sel:WORD_1 dst_unused:UNUSED_PAD src0_sel:DWORD
	v_cvt_i32_f32_e32 v8, v8
	v_lshlrev_b32_e32 v32, 8, v32
	v_lshlrev_b32_e32 v24, 8, v24
	v_lshlrev_b32_e32 v16, 8, v16
	v_and_b32_e32 v32, 0xff00, v32
	v_and_b32_e32 v26, 0xff0000, v26
	v_perm_b32 v28, v28, v30, s79
	v_and_b32_e32 v24, 0xff00, v24
	v_and_b32_e32 v18, 0xff0000, v18
	v_perm_b32 v20, v20, v22, s79
	v_and_b32_e32 v16, 0xff00, v16
	v_and_b32_e32 v10, 0xff0000, v10
	v_perm_b32 v12, v12, v14, s79
	v_lshlrev_b32_e32 v4, 8, v4
	v_or3_b32 v62, v28, v32, v26
	v_or3_b32 v63, v20, v24, v18
	v_or3_b32 v64, v12, v16, v10
	v_and_b32_e32 v4, 0xff00, v4
	v_and_b32_e32 v6, 0xff0000, v6
	v_perm_b32 v2, v8, v2, s79
	s_mov_b64 exec, s[84:85]
	global_store_dwordx4 v[42:43], v[62:65], off offset:384 nt
	s_mov_b64 exec, s[92:93]
	global_store_dwordx4 v[42:43], v[62:65], off offset:384
	s_mov_b64 exec, -1
	v_cvt_f32_f16_e32 v8, v21
	v_mul_f32_e32 v8, v60, v8
	v_or3_b32 v62, v2, v4, v6
	v_cvt_f32_f16_e32 v4, v25
	v_cvt_f32_f16_e32 v2, v23
	v_cvt_f32_f16_e32 v6, v19
	v_rndne_f32_e32 v8, v8
	v_mul_f32_e32 v4, v60, v4
	v_mul_f32_e32 v2, v60, v2
	v_mul_f32_e32 v6, v60, v6
	v_rndne_f32_e32 v4, v4
	v_rndne_f32_e32 v2, v2
	v_cvt_i32_f32_e32 v4, v4
	v_rndne_f32_e32 v6, v6
; template <int NCH>
; __device__ __forceinline__ void quant_colblock(const Frame& F, const float* src, int ld_src, int nvalid, unsigned char* dst, int ld_dst, float* sb) {
;     ...
;     for (int c = 0; c < NCH; ++c) { unsigned t[16][2];
;         if (c < NREG) {
; #pragma unroll
;             for (int i = 0; i < 16; ++i) { t[i][0] = h[c < NREG ? c : 0][i][0]; t[i][1] = h[c < NREG ? c : 0][i][1]; } }
;         else {
; #pragma unroll
;             for (int e = 0; e < 8; ++e) { const u32x4 q = hl[((c - 2) * 8 + e) * 512]; t[2 * e][0] = q.x; t[2 * e][1] = q.y; t[2 * e + 1][0] = q.z; t[2 * e + 1][1] = q.w; } }
; #pragma unroll
;         for (int jn = 0; jn < 4; ++jn) { const float s1 = sc[jn];
;     ...
;             u32x4 o; o.x = pack_i8x4(HV(0), HV(1), HV(2), HV(3)); o.y = pack_i8x4(HV(4), HV(5), HV(6), HV(7)); o.z = pack_i8x4(HV(8), HV(9), HV(10), HV(11)); o.w = pack_i8x4(HV(12), HV(13), HV(14), HV(15));
;     ...
;             *(u32x4*)(db + (size_t)(jn * ld_dst + c * 128) + doff) = o; }
;         __builtin_amdgcn_sched_barrier(0); }
;     __syncthreads();
	v_cvt_i32_f32_e32 v2, v2
	v_cvt_i32_f32_sdwa v6, v6 dst_sel:WORD_1 dst_unused:UNUSED_PAD src0_sel:DWORD
	v_cvt_i32_f32_e32 v8, v8
	v_lshlrev_b32_e32 v4, 8, v4
	v_and_b32_e32 v4, 0xff00, v4
	v_and_b32_e32 v6, 0xff0000, v6
	v_perm_b32 v2, v8, v2, s79
	v_or3_b32 v63, v2, v4, v6
	v_cvt_f32_f16_e32 v4, v17
	v_cvt_f32_f16_e32 v2, v15
	v_cvt_f32_f16_e32 v6, v11
	v_cvt_f32_f16_e32 v8, v13
	v_mul_f32_e32 v4, v60, v4
	v_mul_f32_e32 v2, v60, v2
	v_mul_f32_e32 v6, v60, v6
	v_mul_f32_e32 v8, v60, v8
	v_rndne_f32_e32 v4, v4
	v_rndne_f32_e32 v2, v2
	v_cvt_i32_f32_e32 v4, v4
	v_rndne_f32_e32 v6, v6
	v_rndne_f32_e32 v8, v8
	v_cvt_i32_f32_e32 v2, v2
	v_cvt_i32_f32_sdwa v6, v6 dst_sel:WORD_1 dst_unused:UNUSED_PAD src0_sel:DWORD
	v_cvt_i32_f32_e32 v8, v8
	v_lshlrev_b32_e32 v4, 8, v4
	v_and_b32_e32 v4, 0xff00, v4
	v_and_b32_e32 v6, 0xff0000, v6
	v_perm_b32 v2, v8, v2, s79
	v_or3_b32 v64, v2, v4, v6
	v_cvt_f32_f16_e32 v4, v9
	v_cvt_f32_f16_e32 v2, v7
	v_cvt_f32_f16_e32 v6, v3
	v_cvt_f32_f16_e32 v8, v5
	v_mul_f32_e32 v4, v60, v4
	v_mul_f32_e32 v2, v60, v2
	v_mul_f32_e32 v6, v60, v6
	v_mul_f32_e32 v8, v60, v8
	v_rndne_f32_e32 v4, v4
	v_rndne_f32_e32 v2, v2
	v_cvt_i32_f32_e32 v4, v4
	v_rndne_f32_e32 v6, v6
	v_rndne_f32_e32 v8, v8
	v_cvt_i32_f32_e32 v2, v2
	v_cvt_i32_f32_sdwa v6, v6 dst_sel:WORD_1 dst_unused:UNUSED_PAD src0_sel:DWORD
	v_cvt_i32_f32_e32 v8, v8
	v_lshlrev_b32_e32 v4, 8, v4
	v_and_b32_e32 v4, 0xff00, v4
	v_and_b32_e32 v6, 0xff0000, v6
	v_perm_b32 v2, v8, v2, s79
	v_or3_b32 v65, v2, v4, v6
	v_cvt_f32_f16_sdwa v4, v33 dst_sel:DWORD dst_unused:UNUSED_PAD src0_sel:WORD_1
	v_cvt_f32_f16_sdwa v2, v31 dst_sel:DWORD dst_unused:UNUSED_PAD src0_sel:WORD_1
	v_cvt_f32_f16_sdwa v6, v27 dst_sel:DWORD dst_unused:UNUSED_PAD src0_sel:WORD_1
	v_cvt_f32_f16_sdwa v8, v29 dst_sel:DWORD dst_unused:UNUSED_PAD src0_sel:WORD_1
	v_mul_f32_e32 v4, v34, v4
	v_mul_f32_e32 v2, v34, v2
	v_mul_f32_e32 v6, v34, v6
	v_mul_f32_e32 v8, v34, v8
	v_rndne_f32_e32 v4, v4
	v_rndne_f32_e32 v2, v2
	v_cvt_i32_f32_e32 v4, v4
	v_rndne_f32_e32 v6, v6
	v_rndne_f32_e32 v8, v8
	v_cvt_i32_f32_e32 v2, v2
	v_cvt_i32_f32_sdwa v6, v6 dst_sel:WORD_1 dst_unused:UNUSED_PAD src0_sel:DWORD
	v_cvt_i32_f32_e32 v8, v8
	v_lshlrev_b32_e32 v4, 8, v4
	v_and_b32_e32 v4, 0xff00, v4
	v_and_b32_e32 v6, 0xff0000, v6
	v_perm_b32 v2, v8, v2, s79
	v_or3_b32 v18, v2, v4, v6
	v_cvt_f32_f16_sdwa v4, v25 dst_sel:DWORD dst_unused:UNUSED_PAD src0_sel:WORD_1
	v_cvt_f32_f16_sdwa v2, v23 dst_sel:DWORD dst_unused:UNUSED_PAD src0_sel:WORD_1
	v_cvt_f32_f16_sdwa v6, v19 dst_sel:DWORD dst_unused:UNUSED_PAD src0_sel:WORD_1
	v_cvt_f32_f16_sdwa v8, v21 dst_sel:DWORD dst_unused:UNUSED_PAD src0_sel:WORD_1
	v_mul_f32_e32 v4, v34, v4
	v_mul_f32_e32 v2, v34, v2
	v_mul_f32_e32 v6, v34, v6
	v_mul_f32_e32 v8, v34, v8
	v_rndne_f32_e32 v4, v4
	v_rndne_f32_e32 v2, v2
	v_cvt_i32_f32_e32 v4, v4
	v_rndne_f32_e32 v6, v6
	v_rndne_f32_e32 v8, v8
	v_cvt_i32_f32_e32 v2, v2
	v_cvt_i32_f32_sdwa v6, v6 dst_sel:WORD_1 dst_unused:UNUSED_PAD src0_sel:DWORD
	v_cvt_i32_f32_e32 v8, v8
	v_lshlrev_b32_e32 v4, 8, v4
	v_and_b32_e32 v4, 0xff00, v4
	v_and_b32_e32 v6, 0xff0000, v6
	v_perm_b32 v2, v8, v2, s79
	v_or3_b32 v19, v2, v4, v6
	v_cvt_f32_f16_sdwa v4, v17 dst_sel:DWORD dst_unused:UNUSED_PAD src0_sel:WORD_1
	v_cvt_f32_f16_sdwa v2, v15 dst_sel:DWORD dst_unused:UNUSED_PAD src0_sel:WORD_1
	v_cvt_f32_f16_sdwa v6, v11 dst_sel:DWORD dst_unused:UNUSED_PAD src0_sel:WORD_1
	v_cvt_f32_f16_sdwa v8, v13 dst_sel:DWORD dst_unused:UNUSED_PAD src0_sel:WORD_1
	v_mul_f32_e32 v4, v34, v4
	v_mul_f32_e32 v2, v34, v2
	v_mul_f32_e32 v6, v34, v6
	v_mul_f32_e32 v8, v34, v8
	v_rndne_f32_e32 v4, v4
	v_rndne_f32_e32 v2, v2
	v_cvt_i32_f32_e32 v4, v4
	v_rndne_f32_e32 v6, v6
	v_rndne_f32_e32 v8, v8
	v_cvt_i32_f32_e32 v2, v2
	v_cvt_i32_f32_sdwa v6, v6 dst_sel:WORD_1 dst_unused:UNUSED_PAD src0_sel:DWORD
	v_cvt_i32_f32_e32 v8, v8
	v_lshlrev_b32_e32 v4, 8, v4
	v_and_b32_e32 v4, 0xff00, v4
	v_and_b32_e32 v6, 0xff0000, v6
	v_perm_b32 v2, v8, v2, s79
	v_or3_b32 v20, v2, v4, v6
	v_cvt_f32_f16_sdwa v4, v9 dst_sel:DWORD dst_unused:UNUSED_PAD src0_sel:WORD_1
	v_cvt_f32_f16_sdwa v2, v7 dst_sel:DWORD dst_unused:UNUSED_PAD src0_sel:WORD_1
	v_cvt_f32_f16_sdwa v3, v3 dst_sel:DWORD dst_unused:UNUSED_PAD src0_sel:WORD_1
	v_cvt_f32_f16_sdwa v5, v5 dst_sel:DWORD dst_unused:UNUSED_PAD src0_sel:WORD_1
	v_mul_f32_e32 v4, v34, v4
	v_mul_f32_e32 v2, v34, v2
	v_mul_f32_e32 v3, v34, v3
	v_mul_f32_e32 v5, v34, v5
	v_rndne_f32_e32 v4, v4
	v_rndne_f32_e32 v2, v2
	v_cvt_i32_f32_e32 v4, v4
	v_rndne_f32_e32 v3, v3
	v_rndne_f32_e32 v5, v5
	v_cvt_i32_f32_e32 v2, v2
	v_cvt_i32_f32_sdwa v3, v3 dst_sel:WORD_1 dst_unused:UNUSED_PAD src0_sel:DWORD
	v_cvt_i32_f32_e32 v5, v5
	v_lshlrev_b32_e32 v4, 8, v4
	v_and_b32_e32 v4, 0xff00, v4
	v_and_b32_e32 v3, 0xff0000, v3
	v_perm_b32 v2, v5, v2, s79
	v_or3_b32 v21, v2, v4, v3
	s_mov_b64 exec, s[84:85]
	global_store_dwordx4 v[40:41], v[62:65], off offset:384 nt
	s_mov_b64 exec, s[92:93]
	global_store_dwordx4 v[40:41], v[62:65], off offset:384
	s_mov_b64 exec, -1
	s_mov_b64 exec, s[84:85]
	global_store_dwordx4 v[44:45], v[18:21], off offset:384 nt
	s_mov_b64 exec, s[92:93]
	global_store_dwordx4 v[44:45], v[18:21], off offset:384
	s_mov_b64 exec, -1
	s_add_i32 s82, s82, s96
	s_add_i32 s34, s34, s74
	s_add_i32 s75, s75, s76
	s_add_u32 s36, s36, s38
	s_addc_u32 s37, s37, s39
	s_cmpk_gt_i32 s82, 0x327
	s_barrier
	s_cbranch_scc1 .LBB0_35

; template <int NCH>
; __device__ __forceinline__ void quant_colblock(const Frame& F, const float* src, int ld_src, int nvalid, unsigned char* dst, int ld_dst, float* sb) {
;     ...
;     f32x4 sc; sc.x = am.x > 0.f ? 127.f / am.x : 0.f; sc.y = am.y > 0.f ? 127.f / am.y : 0.f; sc.z = am.z > 0.f ? 127.f / am.z : 0.f; sc.w = am.w > 0.f ? 127.f / am.w : 0.f;
;     if (w == 0 && kg == 0) *(f32x4*)(sb + n) = am * (1.f / 127.f);
;     unsigned char* db = dst + w * rows;
;     const unsigned doff = (unsigned)n * (unsigned)ld_dst + (unsigned)(16 * kg);
; #pragma unroll
;     for (int c = 0; c < NCH; ++c) { unsigned t[16][2];
;         if (c < NREG) {
; #pragma unroll
;             for (int i = 0; i < 16; ++i) { t[i][0] = h[c < NREG ? c : 0][i][0]; t[i][1] = h[c < NREG ? c : 0][i][1]; } }
;         else {
; #pragma unroll
;             for (int e = 0; e < 8; ++e) { const u32x4 q = hl[((c - 2) * 8 + e) * 512]; t[2 * e][0] = q.x; t[2 * e][1] = q.y; t[2 * e + 1][0] = q.z; t[2 * e + 1][1] = q.w; } }
; #pragma unroll
;         for (int jn = 0; jn < 4; ++jn) { const float s1 = sc[jn];
;     ...
;             u32x4 o; o.x = pack_i8x4(HV(0), HV(1), HV(2), HV(3)); o.y = pack_i8x4(HV(4), HV(5), HV(6), HV(7)); o.z = pack_i8x4(HV(8), HV(9), HV(10), HV(11)); o.w = pack_i8x4(HV(12), HV(13), HV(14), HV(15));
;     ...
;             *(u32x4*)(db + (size_t)(jn * ld_dst + c * 128) + doff) = o; }
; __device__ __forceinline__ void phase_prologue(const Frame& F, const Args& a) {
;     ...
;       if (first >= 0) for (int sblk = first; sblk < NSMALL; sblk += span) { const int b = sblk & 127, hi = sblk >> 7;
;           quant_colblock<2>(F, a.in[10 + hi] + 32 * b, D, 32, ws + (hi ? WS_W_UPN : WS_W_UPP) + (size_t)32 * b * 2048, 2048, (float*)(ws + (hi ? SB_UPN : SB_UPP)) + 32 * b); } }
.LBB0_37:
	s_or_b64 exec, exec, s[30:31]
	s_and_b64 s[28:29], s[28:29], exec
	s_cselect_b32 s28, s66, 0x8c00000
	s_add_u32 s30, s4, s28
	v_div_scale_f32 v143, s[28:29], v137, v137, s67
	v_rcp_f32_e32 v144, v143
	s_addc_u32 s31, s5, 0
	s_lshl_b32 s28, s70, 16
	s_add_u32 s30, s30, s28
	v_fma_f32 v145, -v143, v144, 1.0
	v_fmac_f32_e32 v144, v145, v144
	v_div_scale_f32 v145, vcc, s67, v137, s67
	v_mul_f32_e32 v146, v145, v144
	v_fma_f32 v147, -v143, v146, v145
	v_fmac_f32_e32 v146, v147, v144
	v_fma_f32 v143, -v143, v146, v145
	v_div_fmas_f32 v143, v143, v144, v146
	v_div_scale_f32 v144, s[28:29], v136, v136, s67
	v_rcp_f32_e32 v145, v144
	v_div_fixup_f32 v143, v143, v137, s67
	v_cmp_lt_f32_e32 vcc, 0, v137
	v_cvt_pkrtz_f16_f32 v10, v10, v11
	v_cvt_pkrtz_f16_f32 v11, v8, v9
	v_cndmask_b32_e32 v137, 0, v143, vcc
	v_fma_f32 v143, -v144, v145, 1.0
	v_fmac_f32_e32 v145, v143, v145
	v_div_scale_f32 v143, vcc, s67, v136, s67
	v_mul_f32_e32 v146, v143, v145
	v_fma_f32 v147, -v144, v146, v143
	v_fmac_f32_e32 v146, v147, v145
	v_fma_f32 v143, -v144, v146, v143
	v_div_scale_f32 v144, s[28:29], v135, v135, s67
	v_div_fmas_f32 v143, v143, v145, v146
	v_rcp_f32_e32 v145, v144
	v_div_fixup_f32 v143, v143, v136, s67
	v_cmp_lt_f32_e32 vcc, 0, v136
	v_cvt_pkrtz_f16_f32 v9, v2, v3
	v_cvt_pkrtz_f16_f32 v16, v16, v17
	v_cndmask_b32_e32 v136, 0, v143, vcc
	v_fma_f32 v143, -v144, v145, 1.0
	v_fmac_f32_e32 v145, v143, v145
	v_div_scale_f32 v143, vcc, s67, v135, s67
	v_mul_f32_e32 v146, v143, v145
	v_fma_f32 v147, -v144, v146, v143
	v_fmac_f32_e32 v146, v147, v145
	v_fma_f32 v143, -v144, v146, v143
	v_div_scale_f32 v144, s[28:29], v134, v134, s67
	v_div_fmas_f32 v143, v143, v145, v146
	v_rcp_f32_e32 v145, v144
	v_div_fixup_f32 v143, v143, v135, s67
	v_cmp_lt_f32_e32 vcc, 0, v135
	v_cvt_pkrtz_f16_f32 v12, v12, v13
	v_cvt_pkrtz_f16_f32 v8, v6, v7
	v_cndmask_b32_e32 v135, 0, v143, vcc
	v_fma_f32 v143, -v144, v145, 1.0
	v_fmac_f32_e32 v145, v143, v145
	v_div_scale_f32 v143, vcc, s67, v134, s67
	v_mul_f32_e32 v146, v143, v145
	v_fma_f32 v147, -v144, v146, v143
	v_fmac_f32_e32 v146, v147, v145
	v_fma_f32 v143, -v144, v146, v143
	v_cvt_pkrtz_f16_f32 v13, v4, v5
	v_cvt_pkrtz_f16_f32 v17, v18, v19
	v_cvt_f32_f16_e32 v5, v9
	v_div_fmas_f32 v143, v143, v145, v146
	v_cvt_f32_f16_e32 v4, v17
	v_cvt_f32_f16_e32 v6, v8
	v_cvt_f32_f16_e32 v7, v10
	v_div_fixup_f32 v143, v143, v134, s67
	v_cmp_lt_f32_e32 vcc, 0, v134
	v_cvt_pkrtz_f16_f32 v22, v22, v23
	v_cvt_pkrtz_f16_f32 v30, v30, v31
	v_cndmask_b32_e32 v134, 0, v143, vcc
	v_mul_f32_e32 v5, v134, v5
	v_mul_f32_e32 v4, v134, v4
	v_mul_f32_e32 v6, v134, v6
	v_mul_f32_e32 v7, v134, v7
	v_rndne_f32_e32 v5, v5
	v_rndne_f32_e32 v4, v4
	v_cvt_i32_f32_e32 v5, v5
	v_rndne_f32_e32 v6, v6
	v_rndne_f32_e32 v7, v7
	v_cvt_i32_f32_e32 v4, v4
	v_cvt_i32_f32_sdwa v6, v6 dst_sel:WORD_1 dst_unused:UNUSED_PAD src0_sel:DWORD
	v_cvt_i32_f32_e32 v7, v7
	v_lshlrev_b32_e32 v5, 8, v5
	v_and_b32_e32 v5, 0xff00, v5
	v_and_b32_e32 v6, 0xff0000, v6
	v_perm_b32 v4, v7, v4, s68
	v_cvt_pkrtz_f16_f32 v26, v26, v27
	v_cvt_pkrtz_f16_f32 v14, v14, v15
	v_or3_b32 v4, v4, v5, v6
	v_cvt_f32_f16_e32 v6, v22
	v_cvt_f32_f16_e32 v5, v14
	v_cvt_f32_f16_e32 v7, v26
	v_cvt_f32_f16_e32 v18, v30
	v_mul_f32_e32 v6, v134, v6
	v_mul_f32_e32 v5, v134, v5
	v_mul_f32_e32 v7, v134, v7
	v_mul_f32_e32 v18, v134, v18
	v_rndne_f32_e32 v6, v6
	v_rndne_f32_e32 v5, v5
	v_cvt_i32_f32_e32 v6, v6
	v_rndne_f32_e32 v7, v7
	v_rndne_f32_e32 v18, v18
	v_cvt_i32_f32_e32 v5, v5
	v_cvt_i32_f32_sdwa v7, v7 dst_sel:WORD_1 dst_unused:UNUSED_PAD src0_sel:DWORD
	v_cvt_i32_f32_e32 v18, v18
	v_lshlrev_b32_e32 v6, 8, v6
	v_cvt_pkrtz_f16_f32 v38, v38, v39
	v_and_b32_e32 v6, 0xff00, v6
	v_and_b32_e32 v7, 0xff0000, v7
	v_perm_b32 v5, v18, v5, s68
	v_cvt_pkrtz_f16_f32 v46, v46, v47
	v_cvt_pkrtz_f16_f32 v42, v42, v43
	v_cvt_pkrtz_f16_f32 v34, v34, v35
	v_or3_b32 v5, v5, v6, v7
	v_cvt_f32_f16_e32 v7, v38
	v_cvt_f32_f16_e32 v6, v34
	v_cvt_f32_f16_e32 v18, v42
	v_cvt_f32_f16_e32 v19, v46
	v_mul_f32_e32 v7, v134, v7
	v_mul_f32_e32 v6, v134, v6
	v_mul_f32_e32 v18, v134, v18
	v_mul_f32_e32 v19, v134, v19
	v_rndne_f32_e32 v7, v7
	v_rndne_f32_e32 v6, v6
	v_cvt_i32_f32_e32 v7, v7
	v_rndne_f32_e32 v18, v18
	v_rndne_f32_e32 v19, v19
	v_cvt_i32_f32_e32 v6, v6
	v_cvt_i32_f32_sdwa v18, v18 dst_sel:WORD_1 dst_unused:UNUSED_PAD src0_sel:DWORD
	v_cvt_i32_f32_e32 v19, v19
	v_lshlrev_b32_e32 v7, 8, v7
	v_cvt_pkrtz_f16_f32 v54, v54, v55
	v_and_b32_e32 v7, 0xff00, v7
	v_and_b32_e32 v18, 0xff0000, v18
	v_perm_b32 v6, v19, v6, s68
	v_cvt_pkrtz_f16_f32 v62, v62, v63
	v_cvt_pkrtz_f16_f32 v58, v58, v59
	v_cvt_pkrtz_f16_f32 v50, v50, v51
	v_or3_b32 v6, v6, v7, v18
	v_cvt_f32_f16_e32 v18, v54
	v_cvt_pkrtz_f16_f32 v15, v20, v21
	v_cvt_f32_f16_e32 v7, v50
	v_cvt_f32_f16_e32 v19, v58
	v_cvt_f32_f16_e32 v20, v62
	v_mul_f32_e32 v18, v134, v18
	v_mul_f32_e32 v7, v134, v7
	v_mul_f32_e32 v19, v134, v19
	v_mul_f32_e32 v20, v134, v20
	v_rndne_f32_e32 v18, v18
	v_rndne_f32_e32 v7, v7
	v_cvt_i32_f32_e32 v18, v18
	v_rndne_f32_e32 v19, v19
	v_rndne_f32_e32 v20, v20
	v_cvt_i32_f32_e32 v7, v7
	v_cvt_i32_f32_sdwa v19, v19 dst_sel:WORD_1 dst_unused:UNUSED_PAD src0_sel:DWORD
	v_cvt_i32_f32_e32 v20, v20
	s_addc_u32 s31, s31, 0
	s_add_u32 s28, s30, s14
	v_lshlrev_b32_e32 v18, 8, v18
	s_addc_u32 s29, s31, 0
	v_and_b32_e32 v18, 0xff00, v18
	v_and_b32_e32 v19, 0xff0000, v19
	v_perm_b32 v7, v20, v7, s68
	v_lshl_add_u64 v[2:3], s[28:29], 0, v[130:131]
	v_or3_b32 v7, v7, v18, v19
	global_store_dwordx4 v[2:3], v[4:7], off nt
	v_cvt_pkrtz_f16_f32 v24, v24, v25
	v_cvt_pkrtz_f16_f32 v32, v32, v33
	v_cvt_f32_f16_sdwa v5, v9 dst_sel:DWORD dst_unused:UNUSED_PAD src0_sel:WORD_1
; template <int NCH>
; __device__ __forceinline__ void quant_colblock(const Frame& F, const float* src, int ld_src, int nvalid, unsigned char* dst, int ld_dst, float* sb) {
;     ...
;     for (int c = 0; c < NCH; ++c) { unsigned t[16][2];
;         if (c < NREG) {
; #pragma unroll
;             for (int i = 0; i < 16; ++i) { t[i][0] = h[c < NREG ? c : 0][i][0]; t[i][1] = h[c < NREG ? c : 0][i][1]; } }
;         else {
; #pragma unroll
;             for (int e = 0; e < 8; ++e) { const u32x4 q = hl[((c - 2) * 8 + e) * 512]; t[2 * e][0] = q.x; t[2 * e][1] = q.y; t[2 * e + 1][0] = q.z; t[2 * e + 1][1] = q.w; } }
; #pragma unroll
;         for (int jn = 0; jn < 4; ++jn) { const float s1 = sc[jn];
;     ...
;             u32x4 o; o.x = pack_i8x4(HV(0), HV(1), HV(2), HV(3)); o.y = pack_i8x4(HV(4), HV(5), HV(6), HV(7)); o.z = pack_i8x4(HV(8), HV(9), HV(10), HV(11)); o.w = pack_i8x4(HV(12), HV(13), HV(14), HV(15));
;     ...
;             *(u32x4*)(db + (size_t)(jn * ld_dst + c * 128) + doff) = o; }
	v_cvt_f32_f16_sdwa v4, v17 dst_sel:DWORD dst_unused:UNUSED_PAD src0_sel:WORD_1
	v_cvt_f32_f16_sdwa v6, v8 dst_sel:DWORD dst_unused:UNUSED_PAD src0_sel:WORD_1
	v_cvt_f32_f16_sdwa v7, v10 dst_sel:DWORD dst_unused:UNUSED_PAD src0_sel:WORD_1
	v_mul_f32_e32 v5, v135, v5
	v_mul_f32_e32 v4, v135, v4
	v_mul_f32_e32 v6, v135, v6
	v_mul_f32_e32 v7, v135, v7
	v_rndne_f32_e32 v5, v5
	v_rndne_f32_e32 v4, v4
	v_cvt_i32_f32_e32 v5, v5
	v_rndne_f32_e32 v6, v6
	v_rndne_f32_e32 v7, v7
	v_cvt_i32_f32_e32 v4, v4
	v_cvt_i32_f32_sdwa v6, v6 dst_sel:WORD_1 dst_unused:UNUSED_PAD src0_sel:DWORD
	v_cvt_i32_f32_e32 v7, v7
	v_lshlrev_b32_e32 v5, 8, v5
	v_and_b32_e32 v5, 0xff00, v5
	v_and_b32_e32 v6, 0xff0000, v6
	v_perm_b32 v4, v7, v4, s68
	v_or3_b32 v4, v4, v5, v6
	v_cvt_f32_f16_sdwa v6, v22 dst_sel:DWORD dst_unused:UNUSED_PAD src0_sel:WORD_1
	v_cvt_f32_f16_sdwa v5, v14 dst_sel:DWORD dst_unused:UNUSED_PAD src0_sel:WORD_1
	v_cvt_f32_f16_sdwa v7, v26 dst_sel:DWORD dst_unused:UNUSED_PAD src0_sel:WORD_1
	v_cvt_f32_f16_sdwa v8, v30 dst_sel:DWORD dst_unused:UNUSED_PAD src0_sel:WORD_1
	v_mul_f32_e32 v6, v135, v6
	v_mul_f32_e32 v5, v135, v5
	v_mul_f32_e32 v7, v135, v7
	v_mul_f32_e32 v8, v135, v8
	v_rndne_f32_e32 v6, v6
	v_rndne_f32_e32 v5, v5
	v_cvt_i32_f32_e32 v6, v6
	v_rndne_f32_e32 v7, v7
	v_rndne_f32_e32 v8, v8
	v_cvt_i32_f32_e32 v5, v5
	v_cvt_i32_f32_sdwa v7, v7 dst_sel:WORD_1 dst_unused:UNUSED_PAD src0_sel:DWORD
	v_cvt_i32_f32_e32 v8, v8
	v_lshlrev_b32_e32 v6, 8, v6
	v_and_b32_e32 v6, 0xff00, v6
	v_and_b32_e32 v7, 0xff0000, v7
	v_perm_b32 v5, v8, v5, s68
	v_or3_b32 v5, v5, v6, v7
	v_cvt_f32_f16_sdwa v7, v38 dst_sel:DWORD dst_unused:UNUSED_PAD src0_sel:WORD_1
	v_cvt_f32_f16_sdwa v6, v34 dst_sel:DWORD dst_unused:UNUSED_PAD src0_sel:WORD_1
	v_cvt_f32_f16_sdwa v8, v42 dst_sel:DWORD dst_unused:UNUSED_PAD src0_sel:WORD_1
	v_cvt_f32_f16_sdwa v9, v46 dst_sel:DWORD dst_unused:UNUSED_PAD src0_sel:WORD_1
	v_mul_f32_e32 v7, v135, v7
	v_mul_f32_e32 v6, v135, v6
	v_mul_f32_e32 v8, v135, v8
	v_mul_f32_e32 v9, v135, v9
	v_rndne_f32_e32 v7, v7
	v_rndne_f32_e32 v6, v6
	v_cvt_i32_f32_e32 v7, v7
	v_rndne_f32_e32 v8, v8
	v_rndne_f32_e32 v9, v9
	v_cvt_i32_f32_e32 v6, v6
	v_cvt_i32_f32_sdwa v8, v8 dst_sel:WORD_1 dst_unused:UNUSED_PAD src0_sel:DWORD
	v_cvt_i32_f32_e32 v9, v9
	v_lshlrev_b32_e32 v7, 8, v7
	v_and_b32_e32 v7, 0xff00, v7
	v_and_b32_e32 v8, 0xff0000, v8
	v_perm_b32 v6, v9, v6, s68
	v_or3_b32 v6, v6, v7, v8
	v_cvt_f32_f16_sdwa v8, v54 dst_sel:DWORD dst_unused:UNUSED_PAD src0_sel:WORD_1
	v_cvt_f32_f16_sdwa v7, v50 dst_sel:DWORD dst_unused:UNUSED_PAD src0_sel:WORD_1
	v_cvt_f32_f16_sdwa v9, v58 dst_sel:DWORD dst_unused:UNUSED_PAD src0_sel:WORD_1
	v_cvt_f32_f16_sdwa v10, v62 dst_sel:DWORD dst_unused:UNUSED_PAD src0_sel:WORD_1
	v_mul_f32_e32 v8, v135, v8
	v_mul_f32_e32 v7, v135, v7
	v_mul_f32_e32 v9, v135, v9
	v_mul_f32_e32 v10, v135, v10
	v_rndne_f32_e32 v8, v8
	v_rndne_f32_e32 v7, v7
	v_cvt_i32_f32_e32 v8, v8
	v_rndne_f32_e32 v9, v9
	v_rndne_f32_e32 v10, v10
	v_cvt_i32_f32_e32 v7, v7
	v_cvt_i32_f32_sdwa v9, v9 dst_sel:WORD_1 dst_unused:UNUSED_PAD src0_sel:DWORD
	v_cvt_i32_f32_e32 v10, v10
	v_lshlrev_b32_e32 v8, 8, v8
	v_and_b32_e32 v8, 0xff00, v8
	v_and_b32_e32 v9, 0xff0000, v9
	v_perm_b32 v7, v10, v7, s68
	v_or3_b32 v7, v7, v8, v9
	global_store_dwordx4 v[2:3], v[4:7], off offset:2048 nt
	v_cvt_pkrtz_f16_f32 v28, v28, v29
	v_cvt_f32_f16_e32 v8, v32
	v_cvt_f32_f16_e32 v5, v13
	v_cvt_f32_f16_e32 v4, v15
	v_cvt_f32_f16_e32 v6, v11
	v_cvt_f32_f16_e32 v7, v12
	v_mul_f32_e32 v5, v136, v5
	v_mul_f32_e32 v4, v136, v4
	v_mul_f32_e32 v6, v136, v6
	v_mul_f32_e32 v7, v136, v7
	v_rndne_f32_e32 v5, v5
	v_rndne_f32_e32 v4, v4
	v_cvt_i32_f32_e32 v5, v5
	v_rndne_f32_e32 v6, v6
	v_rndne_f32_e32 v7, v7
	v_cvt_i32_f32_e32 v4, v4
	v_cvt_i32_f32_sdwa v6, v6 dst_sel:WORD_1 dst_unused:UNUSED_PAD src0_sel:DWORD
	v_cvt_i32_f32_e32 v7, v7
	v_lshlrev_b32_e32 v5, 8, v5
	v_and_b32_e32 v5, 0xff00, v5
	v_and_b32_e32 v6, 0xff0000, v6
	v_perm_b32 v4, v7, v4, s68
	v_or3_b32 v6, v4, v5, v6
	v_cvt_f32_f16_e32 v5, v24
	v_cvt_f32_f16_e32 v4, v16
	v_cvt_f32_f16_e32 v7, v28
	v_mul_f32_e32 v8, v136, v8
	v_mul_f32_e32 v5, v136, v5
	v_mul_f32_e32 v4, v136, v4
	v_mul_f32_e32 v7, v136, v7
	v_rndne_f32_e32 v5, v5
	v_rndne_f32_e32 v4, v4
	v_cvt_i32_f32_e32 v5, v5
	v_rndne_f32_e32 v7, v7
	v_rndne_f32_e32 v8, v8
	v_cvt_i32_f32_e32 v4, v4
	v_cvt_i32_f32_sdwa v7, v7 dst_sel:WORD_1 dst_unused:UNUSED_PAD src0_sel:DWORD
	v_cvt_i32_f32_e32 v8, v8
	v_lshlrev_b32_e32 v5, 8, v5
	v_cvt_pkrtz_f16_f32 v40, v40, v41
	v_and_b32_e32 v5, 0xff00, v5
	v_and_b32_e32 v7, 0xff0000, v7
	v_perm_b32 v4, v8, v4, s68
	v_cvt_pkrtz_f16_f32 v48, v48, v49
	v_cvt_pkrtz_f16_f32 v44, v44, v45
	v_cvt_pkrtz_f16_f32 v36, v36, v37
	v_or3_b32 v7, v4, v5, v7
	v_cvt_f32_f16_e32 v5, v40
	v_cvt_f32_f16_e32 v4, v36
	v_cvt_f32_f16_e32 v8, v44
	v_cvt_f32_f16_e32 v9, v48
	v_mul_f32_e32 v5, v136, v5
	v_mul_f32_e32 v4, v136, v4
	v_mul_f32_e32 v8, v136, v8
	v_mul_f32_e32 v9, v136, v9
	v_rndne_f32_e32 v5, v5
	v_rndne_f32_e32 v4, v4
	v_cvt_i32_f32_e32 v5, v5
	v_rndne_f32_e32 v8, v8
	v_rndne_f32_e32 v9, v9
	v_cvt_i32_f32_e32 v4, v4
	v_cvt_i32_f32_sdwa v8, v8 dst_sel:WORD_1 dst_unused:UNUSED_PAD src0_sel:DWORD
	v_cvt_i32_f32_e32 v9, v9
	v_lshlrev_b32_e32 v5, 8, v5
	v_cvt_pkrtz_f16_f32 v56, v56, v57
	v_and_b32_e32 v5, 0xff00, v5
	v_and_b32_e32 v8, 0xff0000, v8
	v_perm_b32 v4, v9, v4, s68
	v_cvt_pkrtz_f16_f32 v64, v64, v65
	v_cvt_pkrtz_f16_f32 v60, v60, v61
	v_cvt_pkrtz_f16_f32 v52, v52, v53
	v_or3_b32 v8, v4, v5, v8
	v_cvt_f32_f16_e32 v5, v56
	v_cvt_f32_f16_e32 v4, v52
	v_cvt_f32_f16_e32 v9, v60
	v_cvt_f32_f16_e32 v10, v64
	v_mul_f32_e32 v5, v136, v5
	v_mul_f32_e32 v4, v136, v4
; template <int NCH>
; __device__ __forceinline__ void quant_colblock(const Frame& F, const float* src, int ld_src, int nvalid, unsigned char* dst, int ld_dst, float* sb) {
;     ...
;     for (int c = 0; c < NCH; ++c) { unsigned t[16][2];
;         if (c < NREG) {
; #pragma unroll
;             for (int i = 0; i < 16; ++i) { t[i][0] = h[c < NREG ? c : 0][i][0]; t[i][1] = h[c < NREG ? c : 0][i][1]; } }
;         else {
; #pragma unroll
;             for (int e = 0; e < 8; ++e) { const u32x4 q = hl[((c - 2) * 8 + e) * 512]; t[2 * e][0] = q.x; t[2 * e][1] = q.y; t[2 * e + 1][0] = q.z; t[2 * e + 1][1] = q.w; } }
; #pragma unroll
;         for (int jn = 0; jn < 4; ++jn) { const float s1 = sc[jn];
;     ...
;             u32x4 o; o.x = pack_i8x4(HV(0), HV(1), HV(2), HV(3)); o.y = pack_i8x4(HV(4), HV(5), HV(6), HV(7)); o.z = pack_i8x4(HV(8), HV(9), HV(10), HV(11)); o.w = pack_i8x4(HV(12), HV(13), HV(14), HV(15));
;     ...
;             *(u32x4*)(db + (size_t)(jn * ld_dst + c * 128) + doff) = o; }
	v_mul_f32_e32 v9, v136, v9
	v_mul_f32_e32 v10, v136, v10
	v_rndne_f32_e32 v5, v5
	v_rndne_f32_e32 v4, v4
	v_cvt_i32_f32_e32 v5, v5
	v_rndne_f32_e32 v9, v9
	v_rndne_f32_e32 v10, v10
	v_cvt_i32_f32_e32 v4, v4
	v_cvt_i32_f32_sdwa v9, v9 dst_sel:WORD_1 dst_unused:UNUSED_PAD src0_sel:DWORD
	v_cvt_i32_f32_e32 v10, v10
	v_lshlrev_b32_e32 v5, 8, v5
	v_and_b32_e32 v5, 0xff00, v5
	v_and_b32_e32 v9, 0xff0000, v9
	v_perm_b32 v4, v10, v4, s68
	v_or3_b32 v9, v4, v5, v9
	v_add_co_u32_e32 v4, vcc, s69, v2
	v_cvt_f32_f16_sdwa v10, v32 dst_sel:DWORD dst_unused:UNUSED_PAD src0_sel:WORD_1
	s_nop 0
	v_addc_co_u32_e32 v5, vcc, 0, v3, vcc
	global_store_dwordx4 v[4:5], v[6:9], off nt
	v_mul_f32_e32 v10, v137, v10
	v_rndne_f32_e32 v10, v10
	v_cvt_f32_f16_sdwa v7, v13 dst_sel:DWORD dst_unused:UNUSED_PAD src0_sel:WORD_1
	v_cvt_f32_f16_sdwa v6, v15 dst_sel:DWORD dst_unused:UNUSED_PAD src0_sel:WORD_1
	v_cvt_f32_f16_sdwa v8, v11 dst_sel:DWORD dst_unused:UNUSED_PAD src0_sel:WORD_1
	v_cvt_f32_f16_sdwa v9, v12 dst_sel:DWORD dst_unused:UNUSED_PAD src0_sel:WORD_1
	v_mul_f32_e32 v7, v137, v7
	v_mul_f32_e32 v6, v137, v6
	v_mul_f32_e32 v8, v137, v8
	v_mul_f32_e32 v9, v137, v9
	v_rndne_f32_e32 v7, v7
	v_rndne_f32_e32 v6, v6
	v_cvt_i32_f32_e32 v7, v7
	v_rndne_f32_e32 v8, v8
	v_rndne_f32_e32 v9, v9
	v_cvt_i32_f32_e32 v6, v6
	v_cvt_i32_f32_sdwa v8, v8 dst_sel:WORD_1 dst_unused:UNUSED_PAD src0_sel:DWORD
	v_cvt_i32_f32_e32 v9, v9
	v_lshlrev_b32_e32 v7, 8, v7
	v_and_b32_e32 v7, 0xff00, v7
	v_and_b32_e32 v8, 0xff0000, v8
	v_perm_b32 v6, v9, v6, s68
	v_or3_b32 v6, v6, v7, v8
	v_cvt_f32_f16_sdwa v8, v24 dst_sel:DWORD dst_unused:UNUSED_PAD src0_sel:WORD_1
	v_cvt_f32_f16_sdwa v7, v16 dst_sel:DWORD dst_unused:UNUSED_PAD src0_sel:WORD_1
	v_cvt_f32_f16_sdwa v9, v28 dst_sel:DWORD dst_unused:UNUSED_PAD src0_sel:WORD_1
	v_cvt_i32_f32_e32 v10, v10
	v_mul_f32_e32 v8, v137, v8
	v_mul_f32_e32 v7, v137, v7
	v_mul_f32_e32 v9, v137, v9
	v_rndne_f32_e32 v8, v8
	v_rndne_f32_e32 v7, v7
	v_cvt_i32_f32_e32 v8, v8
	v_rndne_f32_e32 v9, v9
	v_cvt_i32_f32_e32 v7, v7
	v_cvt_i32_f32_sdwa v9, v9 dst_sel:WORD_1 dst_unused:UNUSED_PAD src0_sel:DWORD
	v_lshlrev_b32_e32 v8, 8, v8
	v_and_b32_e32 v8, 0xff00, v8
	v_perm_b32 v7, v10, v7, s68
	v_and_b32_e32 v9, 0xff0000, v9
	v_or3_b32 v7, v7, v8, v9
	v_cvt_f32_f16_sdwa v9, v40 dst_sel:DWORD dst_unused:UNUSED_PAD src0_sel:WORD_1
	v_cvt_f32_f16_sdwa v8, v36 dst_sel:DWORD dst_unused:UNUSED_PAD src0_sel:WORD_1
	v_cvt_f32_f16_sdwa v10, v44 dst_sel:DWORD dst_unused:UNUSED_PAD src0_sel:WORD_1
	v_cvt_f32_f16_sdwa v11, v48 dst_sel:DWORD dst_unused:UNUSED_PAD src0_sel:WORD_1
	v_mul_f32_e32 v9, v137, v9
	v_mul_f32_e32 v8, v137, v8
	v_mul_f32_e32 v10, v137, v10
	v_mul_f32_e32 v11, v137, v11
	v_rndne_f32_e32 v9, v9
	v_rndne_f32_e32 v8, v8
	v_cvt_i32_f32_e32 v9, v9
	v_rndne_f32_e32 v10, v10
	v_rndne_f32_e32 v11, v11
	v_cvt_i32_f32_e32 v8, v8
	v_cvt_i32_f32_sdwa v10, v10 dst_sel:WORD_1 dst_unused:UNUSED_PAD src0_sel:DWORD
	v_cvt_i32_f32_e32 v11, v11
	v_lshlrev_b32_e32 v9, 8, v9
	v_and_b32_e32 v9, 0xff00, v9
	v_and_b32_e32 v10, 0xff0000, v10
	v_perm_b32 v8, v11, v8, s68
	v_or3_b32 v8, v8, v9, v10
	v_cvt_f32_f16_sdwa v10, v56 dst_sel:DWORD dst_unused:UNUSED_PAD src0_sel:WORD_1
	v_cvt_f32_f16_sdwa v9, v52 dst_sel:DWORD dst_unused:UNUSED_PAD src0_sel:WORD_1
	v_cvt_f32_f16_sdwa v11, v60 dst_sel:DWORD dst_unused:UNUSED_PAD src0_sel:WORD_1
	v_cvt_f32_f16_sdwa v12, v64 dst_sel:DWORD dst_unused:UNUSED_PAD src0_sel:WORD_1
	v_mul_f32_e32 v10, v137, v10
	v_mul_f32_e32 v9, v137, v9
	v_mul_f32_e32 v11, v137, v11
	v_mul_f32_e32 v12, v137, v12
	v_rndne_f32_e32 v10, v10
	v_rndne_f32_e32 v9, v9
	v_cvt_i32_f32_e32 v10, v10
	v_rndne_f32_e32 v11, v11
	v_rndne_f32_e32 v12, v12
	v_cvt_i32_f32_e32 v9, v9
	v_cvt_i32_f32_sdwa v11, v11 dst_sel:WORD_1 dst_unused:UNUSED_PAD src0_sel:DWORD
	v_cvt_i32_f32_e32 v12, v12
	v_lshlrev_b32_e32 v10, 8, v10
	v_and_b32_e32 v10, 0xff00, v10
	v_and_b32_e32 v11, 0xff0000, v11
	v_perm_b32 v9, v12, v9, s68
	v_or3_b32 v9, v9, v10, v11
	v_cvt_pkrtz_f16_f32 v128, v128, v129
	v_cvt_pkrtz_f16_f32 v126, v126, v127
	v_cvt_pkrtz_f16_f32 v124, v124, v125
	v_cvt_pkrtz_f16_f32 v122, v122, v123
	v_cvt_pkrtz_f16_f32 v120, v120, v121
	v_cvt_pkrtz_f16_f32 v118, v118, v119
	v_cvt_pkrtz_f16_f32 v116, v116, v117
	v_cvt_pkrtz_f16_f32 v114, v114, v115
	v_cvt_pkrtz_f16_f32 v112, v112, v113
	v_cvt_pkrtz_f16_f32 v110, v110, v111
	v_cvt_pkrtz_f16_f32 v108, v108, v109
	v_cvt_pkrtz_f16_f32 v106, v106, v107
	v_cvt_pkrtz_f16_f32 v104, v104, v105
	v_cvt_pkrtz_f16_f32 v102, v102, v103
	v_cvt_pkrtz_f16_f32 v100, v100, v101
	v_cvt_pkrtz_f16_f32 v98, v98, v99
	v_cvt_pkrtz_f16_f32 v96, v96, v97
	v_cvt_pkrtz_f16_f32 v94, v94, v95
	v_cvt_pkrtz_f16_f32 v92, v92, v93
	v_cvt_pkrtz_f16_f32 v90, v90, v91
	v_cvt_pkrtz_f16_f32 v88, v88, v89
	v_cvt_pkrtz_f16_f32 v86, v86, v87
	v_cvt_pkrtz_f16_f32 v84, v84, v85
	v_cvt_pkrtz_f16_f32 v82, v82, v83
	v_cvt_pkrtz_f16_f32 v80, v80, v81
	v_cvt_pkrtz_f16_f32 v78, v78, v79
	v_cvt_pkrtz_f16_f32 v76, v76, v77
	v_cvt_pkrtz_f16_f32 v74, v74, v75
	v_cvt_pkrtz_f16_f32 v72, v72, v73
	v_cvt_pkrtz_f16_f32 v70, v70, v71
	v_cvt_pkrtz_f16_f32 v68, v68, v69
	v_cvt_pkrtz_f16_f32 v66, v66, v67
	global_store_dwordx4 v[4:5], v[6:9], off offset:2048 nt
	s_nop 1
	v_cvt_f32_f16_e32 v7, v70
	v_cvt_f32_f16_e32 v6, v66
	v_cvt_f32_f16_e32 v8, v74
	v_cvt_f32_f16_e32 v9, v78
	v_mul_f32_e32 v7, v134, v7
	v_mul_f32_e32 v6, v134, v6
	v_mul_f32_e32 v8, v134, v8
	v_mul_f32_e32 v9, v134, v9
	v_rndne_f32_e32 v7, v7
	v_rndne_f32_e32 v6, v6
	v_cvt_i32_f32_e32 v7, v7
	v_rndne_f32_e32 v8, v8
	v_rndne_f32_e32 v9, v9
	v_cvt_i32_f32_e32 v6, v6
	v_cvt_i32_f32_sdwa v8, v8 dst_sel:WORD_1 dst_unused:UNUSED_PAD src0_sel:DWORD
; template <int NCH>
; __device__ __forceinline__ void quant_colblock(const Frame& F, const float* src, int ld_src, int nvalid, unsigned char* dst, int ld_dst, float* sb) {
;     ...
;     for (int c = 0; c < NCH; ++c) { unsigned t[16][2];
;         if (c < NREG) {
; #pragma unroll
;             for (int i = 0; i < 16; ++i) { t[i][0] = h[c < NREG ? c : 0][i][0]; t[i][1] = h[c < NREG ? c : 0][i][1]; } }
;         else {
; #pragma unroll
;             for (int e = 0; e < 8; ++e) { const u32x4 q = hl[((c - 2) * 8 + e) * 512]; t[2 * e][0] = q.x; t[2 * e][1] = q.y; t[2 * e + 1][0] = q.z; t[2 * e + 1][1] = q.w; } }
; #pragma unroll
;         for (int jn = 0; jn < 4; ++jn) { const float s1 = sc[jn];
;     ...
;             u32x4 o; o.x = pack_i8x4(HV(0), HV(1), HV(2), HV(3)); o.y = pack_i8x4(HV(4), HV(5), HV(6), HV(7)); o.z = pack_i8x4(HV(8), HV(9), HV(10), HV(11)); o.w = pack_i8x4(HV(12), HV(13), HV(14), HV(15));
;     ...
;             *(u32x4*)(db + (size_t)(jn * ld_dst + c * 128) + doff) = o; }
	v_cvt_i32_f32_e32 v9, v9
	v_lshlrev_b32_e32 v7, 8, v7
	v_and_b32_e32 v7, 0xff00, v7
	v_and_b32_e32 v8, 0xff0000, v8
	v_perm_b32 v6, v9, v6, s68
	v_or3_b32 v6, v6, v7, v8
	v_cvt_f32_f16_e32 v8, v86
	v_cvt_f32_f16_e32 v7, v82
	v_cvt_f32_f16_e32 v9, v90
	v_cvt_f32_f16_e32 v10, v94
	v_mul_f32_e32 v8, v134, v8
	v_mul_f32_e32 v7, v134, v7
	v_mul_f32_e32 v9, v134, v9
	v_mul_f32_e32 v10, v134, v10
	v_rndne_f32_e32 v8, v8
	v_rndne_f32_e32 v7, v7
	v_cvt_i32_f32_e32 v8, v8
	v_rndne_f32_e32 v9, v9
	v_rndne_f32_e32 v10, v10
	v_cvt_i32_f32_e32 v7, v7
	v_cvt_i32_f32_sdwa v9, v9 dst_sel:WORD_1 dst_unused:UNUSED_PAD src0_sel:DWORD
	v_cvt_i32_f32_e32 v10, v10
	v_lshlrev_b32_e32 v8, 8, v8
	v_and_b32_e32 v8, 0xff00, v8
	v_and_b32_e32 v9, 0xff0000, v9
	v_perm_b32 v7, v10, v7, s68
	v_or3_b32 v7, v7, v8, v9
	v_cvt_f32_f16_e32 v9, v102
	v_cvt_f32_f16_e32 v8, v98
	v_cvt_f32_f16_e32 v10, v106
	v_cvt_f32_f16_e32 v11, v110
	v_mul_f32_e32 v9, v134, v9
	v_mul_f32_e32 v8, v134, v8
	v_mul_f32_e32 v10, v134, v10
	v_mul_f32_e32 v11, v134, v11
	v_rndne_f32_e32 v9, v9
	v_rndne_f32_e32 v8, v8
	v_cvt_i32_f32_e32 v9, v9
	v_rndne_f32_e32 v10, v10
	v_rndne_f32_e32 v11, v11
	v_cvt_i32_f32_e32 v8, v8
	v_cvt_i32_f32_sdwa v10, v10 dst_sel:WORD_1 dst_unused:UNUSED_PAD src0_sel:DWORD
	v_cvt_i32_f32_e32 v11, v11
	v_lshlrev_b32_e32 v9, 8, v9
	v_and_b32_e32 v9, 0xff00, v9
	v_and_b32_e32 v10, 0xff0000, v10
	v_perm_b32 v8, v11, v8, s68
	v_or3_b32 v8, v8, v9, v10
	v_cvt_f32_f16_e32 v10, v118
	v_cvt_f32_f16_e32 v9, v114
	v_cvt_f32_f16_e32 v11, v122
	v_cvt_f32_f16_e32 v12, v126
	v_mul_f32_e32 v10, v134, v10
	v_mul_f32_e32 v9, v134, v9
	v_mul_f32_e32 v11, v134, v11
	v_mul_f32_e32 v12, v134, v12
	v_rndne_f32_e32 v10, v10
	v_rndne_f32_e32 v9, v9
	v_cvt_i32_f32_e32 v10, v10
	v_rndne_f32_e32 v11, v11
	v_rndne_f32_e32 v12, v12
	v_cvt_i32_f32_e32 v9, v9
	v_cvt_i32_f32_sdwa v11, v11 dst_sel:WORD_1 dst_unused:UNUSED_PAD src0_sel:DWORD
	v_cvt_i32_f32_e32 v12, v12
	v_lshlrev_b32_e32 v10, 8, v10
	v_and_b32_e32 v10, 0xff00, v10
	v_and_b32_e32 v11, 0xff0000, v11
	v_perm_b32 v9, v12, v9, s68
	v_or3_b32 v9, v9, v10, v11
	global_store_dwordx4 v[2:3], v[6:9], off offset:128 nt
	v_cvt_f32_f16_sdwa v10, v94 dst_sel:DWORD dst_unused:UNUSED_PAD src0_sel:WORD_1
	v_cvt_f32_f16_sdwa v11, v110 dst_sel:DWORD dst_unused:UNUSED_PAD src0_sel:WORD_1
	v_cvt_f32_f16_sdwa v7, v70 dst_sel:DWORD dst_unused:UNUSED_PAD src0_sel:WORD_1
	v_cvt_f32_f16_sdwa v6, v66 dst_sel:DWORD dst_unused:UNUSED_PAD src0_sel:WORD_1
	v_cvt_f32_f16_sdwa v8, v74 dst_sel:DWORD dst_unused:UNUSED_PAD src0_sel:WORD_1
	v_cvt_f32_f16_sdwa v9, v78 dst_sel:DWORD dst_unused:UNUSED_PAD src0_sel:WORD_1
	v_mul_f32_e32 v7, v135, v7
	v_mul_f32_e32 v6, v135, v6
	v_mul_f32_e32 v8, v135, v8
	v_mul_f32_e32 v9, v135, v9
	v_rndne_f32_e32 v7, v7
	v_rndne_f32_e32 v6, v6
	v_cvt_i32_f32_e32 v7, v7
	v_rndne_f32_e32 v8, v8
	v_rndne_f32_e32 v9, v9
	v_cvt_i32_f32_e32 v6, v6
	v_cvt_i32_f32_sdwa v8, v8 dst_sel:WORD_1 dst_unused:UNUSED_PAD src0_sel:DWORD
	v_cvt_i32_f32_e32 v9, v9
	v_lshlrev_b32_e32 v7, 8, v7
	v_and_b32_e32 v7, 0xff00, v7
	v_and_b32_e32 v8, 0xff0000, v8
	v_perm_b32 v6, v9, v6, s68
	v_or3_b32 v6, v6, v7, v8
	v_cvt_f32_f16_sdwa v8, v86 dst_sel:DWORD dst_unused:UNUSED_PAD src0_sel:WORD_1
	v_cvt_f32_f16_sdwa v7, v82 dst_sel:DWORD dst_unused:UNUSED_PAD src0_sel:WORD_1
	v_cvt_f32_f16_sdwa v9, v90 dst_sel:DWORD dst_unused:UNUSED_PAD src0_sel:WORD_1
	v_mul_f32_e32 v10, v135, v10
	v_mul_f32_e32 v8, v135, v8
	v_mul_f32_e32 v7, v135, v7
	v_mul_f32_e32 v9, v135, v9
	v_rndne_f32_e32 v8, v8
	v_rndne_f32_e32 v7, v7
	v_cvt_i32_f32_e32 v8, v8
	v_rndne_f32_e32 v9, v9
	v_rndne_f32_e32 v10, v10
	v_cvt_i32_f32_e32 v7, v7
	v_cvt_i32_f32_sdwa v9, v9 dst_sel:WORD_1 dst_unused:UNUSED_PAD src0_sel:DWORD
	v_cvt_i32_f32_e32 v10, v10
	v_lshlrev_b32_e32 v8, 8, v8
	v_and_b32_e32 v8, 0xff00, v8
	v_and_b32_e32 v9, 0xff0000, v9
	v_perm_b32 v7, v10, v7, s68
	v_or3_b32 v7, v7, v8, v9
	v_cvt_f32_f16_sdwa v9, v102 dst_sel:DWORD dst_unused:UNUSED_PAD src0_sel:WORD_1
	v_cvt_f32_f16_sdwa v8, v98 dst_sel:DWORD dst_unused:UNUSED_PAD src0_sel:WORD_1
	v_cvt_f32_f16_sdwa v10, v106 dst_sel:DWORD dst_unused:UNUSED_PAD src0_sel:WORD_1
	v_mul_f32_e32 v11, v135, v11
	v_mul_f32_e32 v9, v135, v9
	v_mul_f32_e32 v8, v135, v8
	v_mul_f32_e32 v10, v135, v10
	v_rndne_f32_e32 v9, v9
	v_rndne_f32_e32 v8, v8
	v_cvt_i32_f32_e32 v9, v9
	v_rndne_f32_e32 v10, v10
	v_rndne_f32_e32 v11, v11
	v_cvt_i32_f32_e32 v8, v8
	v_cvt_i32_f32_sdwa v10, v10 dst_sel:WORD_1 dst_unused:UNUSED_PAD src0_sel:DWORD
	v_cvt_i32_f32_e32 v11, v11
	v_lshlrev_b32_e32 v9, 8, v9
	v_and_b32_e32 v9, 0xff00, v9
	v_and_b32_e32 v10, 0xff0000, v10
	v_perm_b32 v8, v11, v8, s68
	v_or3_b32 v8, v8, v9, v10
	v_cvt_f32_f16_sdwa v10, v118 dst_sel:DWORD dst_unused:UNUSED_PAD src0_sel:WORD_1
	v_cvt_f32_f16_sdwa v9, v114 dst_sel:DWORD dst_unused:UNUSED_PAD src0_sel:WORD_1
	v_cvt_f32_f16_sdwa v11, v122 dst_sel:DWORD dst_unused:UNUSED_PAD src0_sel:WORD_1
	v_cvt_f32_f16_sdwa v12, v126 dst_sel:DWORD dst_unused:UNUSED_PAD src0_sel:WORD_1
	v_mul_f32_e32 v10, v135, v10
	v_mul_f32_e32 v9, v135, v9
	v_mul_f32_e32 v11, v135, v11
	v_mul_f32_e32 v12, v135, v12
	v_rndne_f32_e32 v10, v10
	v_rndne_f32_e32 v9, v9
	v_cvt_i32_f32_e32 v10, v10
	v_rndne_f32_e32 v11, v11
	v_rndne_f32_e32 v12, v12
	v_cvt_i32_f32_e32 v9, v9
	v_cvt_i32_f32_sdwa v11, v11 dst_sel:WORD_1 dst_unused:UNUSED_PAD src0_sel:DWORD
	v_cvt_i32_f32_e32 v12, v12
	v_lshlrev_b32_e32 v10, 8, v10
	v_and_b32_e32 v10, 0xff00, v10
	v_and_b32_e32 v11, 0xff0000, v11
	v_perm_b32 v9, v12, v9, s68
	v_or3_b32 v9, v9, v10, v11
	global_store_dwordx4 v[2:3], v[6:9], off offset:2176 nt
	v_cvt_f32_f16_e32 v3, v72
	v_cvt_f32_f16_e32 v2, v68
; template <int NCH>
; __device__ __forceinline__ void quant_colblock(const Frame& F, const float* src, int ld_src, int nvalid, unsigned char* dst, int ld_dst, float* sb) {
;     ...
;     for (int c = 0; c < NCH; ++c) { unsigned t[16][2];
;         if (c < NREG) {
; #pragma unroll
;             for (int i = 0; i < 16; ++i) { t[i][0] = h[c < NREG ? c : 0][i][0]; t[i][1] = h[c < NREG ? c : 0][i][1]; } }
;         else {
; #pragma unroll
;             for (int e = 0; e < 8; ++e) { const u32x4 q = hl[((c - 2) * 8 + e) * 512]; t[2 * e][0] = q.x; t[2 * e][1] = q.y; t[2 * e + 1][0] = q.z; t[2 * e + 1][1] = q.w; } }
; #pragma unroll
;         for (int jn = 0; jn < 4; ++jn) { const float s1 = sc[jn];
;     ...
;             u32x4 o; o.x = pack_i8x4(HV(0), HV(1), HV(2), HV(3)); o.y = pack_i8x4(HV(4), HV(5), HV(6), HV(7)); o.z = pack_i8x4(HV(8), HV(9), HV(10), HV(11)); o.w = pack_i8x4(HV(12), HV(13), HV(14), HV(15));
;     ...
;             *(u32x4*)(db + (size_t)(jn * ld_dst + c * 128) + doff) = o; }
;         __builtin_amdgcn_sched_barrier(0); }
; __device__ __forceinline__ void phase_prologue(const Frame& F, const Args& a) {
;     ...
;       if (first >= 0) for (int sblk = first; sblk < NSMALL; sblk += span) { const int b = sblk & 127, hi = sblk >> 7;
	v_cvt_f32_f16_e32 v6, v76
	v_cvt_f32_f16_e32 v7, v80
	v_mul_f32_e32 v3, v136, v3
	v_mul_f32_e32 v2, v136, v2
	v_mul_f32_e32 v6, v136, v6
	v_mul_f32_e32 v7, v136, v7
	v_rndne_f32_e32 v3, v3
	v_rndne_f32_e32 v2, v2
	v_cvt_i32_f32_e32 v3, v3
	v_rndne_f32_e32 v6, v6
	v_rndne_f32_e32 v7, v7
	v_cvt_i32_f32_e32 v2, v2
	v_cvt_i32_f32_sdwa v6, v6 dst_sel:WORD_1 dst_unused:UNUSED_PAD src0_sel:DWORD
	v_cvt_i32_f32_e32 v7, v7
	v_lshlrev_b32_e32 v3, 8, v3
	v_and_b32_e32 v3, 0xff00, v3
	v_and_b32_e32 v6, 0xff0000, v6
	v_perm_b32 v2, v7, v2, s68
	v_or3_b32 v6, v2, v3, v6
	v_cvt_f32_f16_e32 v3, v88
	v_cvt_f32_f16_e32 v2, v84
	v_cvt_f32_f16_e32 v7, v92
	v_cvt_f32_f16_e32 v8, v96
	v_mul_f32_e32 v3, v136, v3
	v_mul_f32_e32 v2, v136, v2
	v_mul_f32_e32 v7, v136, v7
	v_mul_f32_e32 v8, v136, v8
	v_rndne_f32_e32 v3, v3
	v_rndne_f32_e32 v2, v2
	v_cvt_i32_f32_e32 v3, v3
	v_rndne_f32_e32 v7, v7
	v_rndne_f32_e32 v8, v8
	v_cvt_i32_f32_e32 v2, v2
	v_cvt_i32_f32_sdwa v7, v7 dst_sel:WORD_1 dst_unused:UNUSED_PAD src0_sel:DWORD
	v_cvt_i32_f32_e32 v8, v8
	v_lshlrev_b32_e32 v3, 8, v3
	v_and_b32_e32 v3, 0xff00, v3
	v_and_b32_e32 v7, 0xff0000, v7
	v_perm_b32 v2, v8, v2, s68
	v_or3_b32 v7, v2, v3, v7
	v_cvt_f32_f16_e32 v3, v104
	v_cvt_f32_f16_e32 v2, v100
	v_cvt_f32_f16_e32 v8, v108
	v_cvt_f32_f16_e32 v9, v112
	v_mul_f32_e32 v3, v136, v3
	v_mul_f32_e32 v2, v136, v2
	v_mul_f32_e32 v8, v136, v8
	v_mul_f32_e32 v9, v136, v9
	v_rndne_f32_e32 v3, v3
	v_rndne_f32_e32 v2, v2
	v_cvt_i32_f32_e32 v3, v3
	v_rndne_f32_e32 v8, v8
	v_rndne_f32_e32 v9, v9
	v_cvt_i32_f32_e32 v2, v2
	v_cvt_i32_f32_sdwa v8, v8 dst_sel:WORD_1 dst_unused:UNUSED_PAD src0_sel:DWORD
	v_cvt_i32_f32_e32 v9, v9
	v_lshlrev_b32_e32 v3, 8, v3
	v_and_b32_e32 v3, 0xff00, v3
	v_and_b32_e32 v8, 0xff0000, v8
	v_perm_b32 v2, v9, v2, s68
	v_or3_b32 v8, v2, v3, v8
	v_cvt_f32_f16_e32 v3, v120
	v_cvt_f32_f16_e32 v2, v116
	v_cvt_f32_f16_e32 v9, v124
	v_cvt_f32_f16_e32 v10, v128
	v_mul_f32_e32 v3, v136, v3
	v_mul_f32_e32 v2, v136, v2
	v_mul_f32_e32 v9, v136, v9
	v_mul_f32_e32 v10, v136, v10
	v_rndne_f32_e32 v3, v3
	v_rndne_f32_e32 v2, v2
	v_cvt_i32_f32_e32 v3, v3
	v_rndne_f32_e32 v9, v9
	v_rndne_f32_e32 v10, v10
	v_cvt_i32_f32_e32 v2, v2
	v_cvt_i32_f32_sdwa v9, v9 dst_sel:WORD_1 dst_unused:UNUSED_PAD src0_sel:DWORD
	v_cvt_i32_f32_e32 v10, v10
	v_lshlrev_b32_e32 v3, 8, v3
	v_and_b32_e32 v3, 0xff00, v3
	v_and_b32_e32 v9, 0xff0000, v9
	v_perm_b32 v2, v10, v2, s68
	v_or3_b32 v9, v2, v3, v9
	v_cvt_f32_f16_sdwa v3, v72 dst_sel:DWORD dst_unused:UNUSED_PAD src0_sel:WORD_1
	global_store_dwordx4 v[4:5], v[6:9], off offset:128 nt
	v_cvt_f32_f16_sdwa v2, v68 dst_sel:DWORD dst_unused:UNUSED_PAD src0_sel:WORD_1
	v_cvt_f32_f16_sdwa v10, v128 dst_sel:DWORD dst_unused:UNUSED_PAD src0_sel:WORD_1
	v_cvt_f32_f16_sdwa v6, v76 dst_sel:DWORD dst_unused:UNUSED_PAD src0_sel:WORD_1
	v_cvt_f32_f16_sdwa v7, v80 dst_sel:DWORD dst_unused:UNUSED_PAD src0_sel:WORD_1
	v_mul_f32_e32 v3, v137, v3
	v_mul_f32_e32 v2, v137, v2
	v_mul_f32_e32 v6, v137, v6
	v_mul_f32_e32 v7, v137, v7
	v_rndne_f32_e32 v3, v3
	v_rndne_f32_e32 v2, v2
	v_cvt_i32_f32_e32 v3, v3
	v_rndne_f32_e32 v6, v6
	v_rndne_f32_e32 v7, v7
	v_cvt_i32_f32_e32 v2, v2
	v_cvt_i32_f32_sdwa v6, v6 dst_sel:WORD_1 dst_unused:UNUSED_PAD src0_sel:DWORD
	v_cvt_i32_f32_e32 v7, v7
	v_lshlrev_b32_e32 v3, 8, v3
	v_and_b32_e32 v3, 0xff00, v3
	v_and_b32_e32 v6, 0xff0000, v6
	v_perm_b32 v2, v7, v2, s68
	v_or3_b32 v6, v2, v3, v6
	v_cvt_f32_f16_sdwa v3, v88 dst_sel:DWORD dst_unused:UNUSED_PAD src0_sel:WORD_1
	v_cvt_f32_f16_sdwa v2, v84 dst_sel:DWORD dst_unused:UNUSED_PAD src0_sel:WORD_1
	v_cvt_f32_f16_sdwa v7, v92 dst_sel:DWORD dst_unused:UNUSED_PAD src0_sel:WORD_1
	v_cvt_f32_f16_sdwa v8, v96 dst_sel:DWORD dst_unused:UNUSED_PAD src0_sel:WORD_1
	v_mul_f32_e32 v3, v137, v3
	v_mul_f32_e32 v2, v137, v2
	v_mul_f32_e32 v7, v137, v7
	v_mul_f32_e32 v8, v137, v8
	v_rndne_f32_e32 v3, v3
	v_rndne_f32_e32 v2, v2
	v_cvt_i32_f32_e32 v3, v3
	v_rndne_f32_e32 v7, v7
	v_rndne_f32_e32 v8, v8
	v_cvt_i32_f32_e32 v2, v2
	v_cvt_i32_f32_sdwa v7, v7 dst_sel:WORD_1 dst_unused:UNUSED_PAD src0_sel:DWORD
	v_cvt_i32_f32_e32 v8, v8
	v_lshlrev_b32_e32 v3, 8, v3
	v_and_b32_e32 v3, 0xff00, v3
	v_and_b32_e32 v7, 0xff0000, v7
	v_perm_b32 v2, v8, v2, s68
	v_or3_b32 v7, v2, v3, v7
	v_cvt_f32_f16_sdwa v3, v104 dst_sel:DWORD dst_unused:UNUSED_PAD src0_sel:WORD_1
	v_cvt_f32_f16_sdwa v2, v100 dst_sel:DWORD dst_unused:UNUSED_PAD src0_sel:WORD_1
	v_cvt_f32_f16_sdwa v8, v108 dst_sel:DWORD dst_unused:UNUSED_PAD src0_sel:WORD_1
	v_cvt_f32_f16_sdwa v9, v112 dst_sel:DWORD dst_unused:UNUSED_PAD src0_sel:WORD_1
	v_mul_f32_e32 v3, v137, v3
	v_mul_f32_e32 v2, v137, v2
	v_mul_f32_e32 v8, v137, v8
	v_mul_f32_e32 v9, v137, v9
	v_rndne_f32_e32 v3, v3
	v_rndne_f32_e32 v2, v2
	v_cvt_i32_f32_e32 v3, v3
	v_rndne_f32_e32 v8, v8
	v_rndne_f32_e32 v9, v9
	v_cvt_i32_f32_e32 v2, v2
	v_cvt_i32_f32_sdwa v8, v8 dst_sel:WORD_1 dst_unused:UNUSED_PAD src0_sel:DWORD
	v_cvt_i32_f32_e32 v9, v9
	v_lshlrev_b32_e32 v3, 8, v3
	v_and_b32_e32 v3, 0xff00, v3
	v_and_b32_e32 v8, 0xff0000, v8
	v_perm_b32 v2, v9, v2, s68
	v_or3_b32 v8, v2, v3, v8
	v_cvt_f32_f16_sdwa v3, v120 dst_sel:DWORD dst_unused:UNUSED_PAD src0_sel:WORD_1
	v_cvt_f32_f16_sdwa v2, v116 dst_sel:DWORD dst_unused:UNUSED_PAD src0_sel:WORD_1
	v_cvt_f32_f16_sdwa v9, v124 dst_sel:DWORD dst_unused:UNUSED_PAD src0_sel:WORD_1
	v_mul_f32_e32 v10, v137, v10
	v_mul_f32_e32 v3, v137, v3
	v_mul_f32_e32 v2, v137, v2
	v_mul_f32_e32 v9, v137, v9
	v_rndne_f32_e32 v3, v3
	v_rndne_f32_e32 v2, v2
	v_cvt_i32_f32_e32 v3, v3
	v_rndne_f32_e32 v9, v9
	v_rndne_f32_e32 v10, v10
	v_cvt_i32_f32_e32 v2, v2
	v_cvt_i32_f32_sdwa v9, v9 dst_sel:WORD_1 dst_unused:UNUSED_PAD src0_sel:DWORD
	v_cvt_i32_f32_e32 v10, v10
	v_lshlrev_b32_e32 v3, 8, v3
	v_and_b32_e32 v3, 0xff00, v3
	v_and_b32_e32 v9, 0xff0000, v9
	v_perm_b32 v2, v10, v2, s68
	v_or3_b32 v9, v2, v3, v9
	global_store_dwordx4 v[4:5], v[6:9], off offset:2176 nt
	s_add_i32 s21, s21, s34
	s_cmpk_lt_i32 s21, 0x100
	s_barrier
	s_cbranch_scc0 .LBB0_42
